# baseline (speedup 1.0000x reference)
_Z16bilateral_kernelPKfS0_Pf:
	s_load_dwordx2 s[4:5], s[0:1], 0x0
	s_load_dwordx2 s[8:9], s[0:1], 0x10
	s_and_b32 s0, s2, 7
	s_mulk_i32 s0, 0x60
	s_lshr_b32 s1, s2, 3
	s_add_i32 s1, s0, s1
	s_lshr_b32 s0, s1, 6
	s_lshl_b32 s11, s1, 6
	s_and_b32 s11, s11, 0x1c0
	s_lshl_b32 s1, s1, 3
	s_nop 0
	s_and_b32 s10, s1, 0x1c0
	s_mov_b32 s1, 0
	s_lshl_b64 s[2:3], s[0:1], 20
	s_mov_b32 s20, 0xc05dfbe6
	s_mov_b32 s21, 0xc05dfbe6
	s_mov_b32 s22, 0xc0a8390e
	s_mov_b32 s23, 0xc0a8390e
	s_mov_b32 s24, 0xc08211a7
	s_mov_b32 s25, 0xc08211a7
	s_mov_b32 s26, 0xc0bb4cc1
	s_mov_b32 s27, 0xc0bb4cc1
	s_mov_b32 s28, 0xc0f487dc
	s_mov_b32 s29, 0xc0f487dc
	s_mov_b32 s30, 0x3e0bd796
	s_mov_b32 s31, 0x3e0bd796
	s_mov_b32 s32, 0x3f45a90c
	s_mov_b32 s33, 0x3f45a90c
	s_mov_b32 s34, 0x3fa5c782
	s_mov_b32 s35, 0x3fa5c782
	v_and_b32_e32 v118, 15, v0
	v_lshrrev_b32_e32 v115, 2, v0
	v_lshl_or_b32 v113, v118, 2, s11
	v_and_or_b32 v117, v115, 60, s10
	v_min_u32_e32 v116, 0x1fa, v113
	v_sub_u32_e64 v115, v113, 2 clamp
	v_add_u32_e64 v116, 4, v116
	v_cmp_eq_u32_e64 s[16:17], 0, v118
	v_cmp_eq_u32_e32 vcc, 15, v118
	s_nop 1
	v_cndmask_b32_e64 v115, v116, v115, s[16:17]
	s_or_b64 vcc, s[16:17], vcc
	v_lshlrev_b32_e32 v115, 2, v115
	v_mov_b32_e32 v116, 0x7ff00000
	s_nop 0
	v_cndmask_b32_e32 v112, v116, v115, vcc
	s_movk_i32 s18, 0x1fc
	v_cmp_eq_u32_e32 vcc, 0, v113
	v_cmp_eq_u32_e64 s[16:17], s18, v113
	v_lshlrev_b32_e32 v113, 2, v113
	s_waitcnt lgkmcnt(0)
	s_add_u32 s4, s4, s2
	s_addc_u32 s5, s5, s3
	s_and_b32 s5, s5, 0xffff
	s_mov_b32 s6, 0x100000
	s_mov_b32 s7, 0x20000
	s_add_u32 s12, s8, s2
	s_addc_u32 s13, s9, s3
	s_and_b32 s13, s13, 0xffff
	s_mov_b32 s14, 0x100000
	s_mov_b32 s15, 0x20000
	v_lshlrev_b32_e32 v115, 11, v117
	v_add_u32_e32 v116, v115, v112
	v_add_u32_e64 v114, v115, v113
	v_add_u32_e32 v119, 0x1000, v114
	buffer_load_dwordx2 v[16:17], v116, s[4:7], 0 offen nt
	buffer_load_dwordx2 v[22:23], v116, s[4:7], 0 offen nt
	buffer_load_dwordx4 v[18:21], v114, s[4:7], 0 offen nt
	v_lshlrev_b32_e64 v115, 11, v117
	v_add_u32_e32 v115, 0x800, v115
	v_add_u32_e32 v116, v115, v112
	v_add_u32_e32 v115, v115, v113
	buffer_load_dwordx2 v[24:25], v116, s[4:7], 0 offen nt
	buffer_load_dwordx2 v[30:31], v116, s[4:7], 0 offen nt
	buffer_load_dwordx4 v[26:29], v115, s[4:7], 0 offen nt
	v_sub_u32_e64 v115, v117, 1 clamp
	v_lshlrev_b32_e32 v115, 11, v115
	v_add_u32_e32 v116, v115, v112
	v_add_u32_e64 v115, v115, v113
	buffer_load_dwordx2 v[8:9], v116, s[4:7], 0 offen nt
	buffer_load_dwordx2 v[14:15], v116, s[4:7], 0 offen nt
	buffer_load_dwordx4 v[10:13], v115, s[4:7], 0 offen nt
	v_lshlrev_b32_e64 v115, 11, v117
	v_add_u32_e32 v115, 0x1000, v115
	v_add_u32_e32 v116, v115, v112
	v_add_u32_e32 v115, v115, v113
	buffer_load_dwordx2 v[32:33], v116, s[4:7], 0 offen nt
	buffer_load_dwordx2 v[38:39], v116, s[4:7], 0 offen nt
	buffer_load_dwordx4 v[34:37], v115, s[4:7], 0 offen nt
	v_sub_u32_e64 v115, v117, 2 clamp
	v_lshlrev_b32_e32 v115, 11, v115
	v_add_u32_e32 v116, v115, v112
	v_add_u32_e64 v115, v115, v113
	buffer_load_dwordx2 v[0:1], v116, s[4:7], 0 offen nt
	buffer_load_dwordx2 v[6:7], v116, s[4:7], 0 offen nt
	buffer_load_dwordx4 v[2:5], v115, s[4:7], 0 offen nt
	v_lshlrev_b32_e64 v115, 11, v117
	v_add_u32_e32 v115, 0x1800, v115
	v_add_u32_e32 v116, v115, v112
	v_add_u32_e32 v115, v115, v113
	buffer_load_dwordx2 v[40:41], v116, s[4:7], 0 offen nt
	buffer_load_dwordx2 v[46:47], v116, s[4:7], 0 offen nt
	buffer_load_dwordx4 v[42:45], v115, s[4:7], 0 offen nt
	v_min_u32_e32 v115, 0x1fb, v117
	v_lshlrev_b32_e64 v115, 11, v115
	v_add_u32_e32 v115, 0x2000, v115
	v_add_u32_e32 v116, v115, v112
	v_add_u32_e32 v115, v115, v113
	buffer_load_dwordx2 v[48:49], v116, s[4:7], 0 offen nt
	buffer_load_dwordx2 v[54:55], v116, s[4:7], 0 offen nt
	buffer_load_dwordx4 v[50:53], v115, s[4:7], 0 offen nt
	v_min_u32_e32 v115, 0x1fa, v117
	v_lshlrev_b32_e64 v115, 11, v115
	v_add_u32_e32 v115, 0x2800, v115
	v_add_u32_e32 v116, v115, v112
	v_add_u32_e32 v115, v115, v113
	buffer_load_dwordx2 v[56:57], v116, s[4:7], 0 offen nt
	buffer_load_dwordx2 v[62:63], v116, s[4:7], 0 offen nt
	buffer_load_dwordx4 v[58:61], v115, s[4:7], 0 offen nt
	s_waitcnt vmcnt(21)
	s_nop 0
	v_mov_b32_dpp v16, v20 row_shr:1 row_mask:0xf bank_mask:0xf
	v_mov_b32_dpp v17, v21 row_shr:1 row_mask:0xf bank_mask:0xf
	v_mov_b32_dpp v22, v18 row_shl:1 row_mask:0xf bank_mask:0xf
	v_mov_b32_dpp v23, v19 row_shl:1 row_mask:0xf bank_mask:0xf
	v_pk_mul_f32 v[18:19], v[18:19], s[32:33]
	v_pk_mul_f32 v[20:21], v[20:21], s[32:33]
	v_cndmask_b32_e64 v17, v17, v16, vcc
	v_cndmask_b32_e64 v22, v22, v23, s[16:17]
	v_pk_mul_f32 v[68:69], v[18:19], s[30:31]
	v_pk_mul_f32 v[70:71], v[20:21], s[30:31]
	v_pk_mul_f32 v[16:17], v[16:17], s[32:33]
	v_pk_mul_f32 v[22:23], v[22:23], s[32:33]
	v_mov_b32_e32 v64, s30
	v_mov_b32_e32 v65, s30
	v_mov_b32_e64 v66, s30
	v_mov_b32_e32 v67, s30
	s_setprio 3
	v_pk_add_f32 v[96:97], v[18:19], v[16:17] neg_lo:[0,1] neg_hi:[0,1]
	v_pk_add_f32 v[98:99], v[20:21], v[18:19] neg_lo:[0,1] neg_hi:[0,1]
	v_pk_add_f32 v[100:101], v[22:23], v[20:21] neg_lo:[0,1] neg_hi:[0,1]
	v_pk_fma_f32 v[96:97], v[96:97], v[96:97], s[22:23] neg_lo:[1,0,0] neg_hi:[1,0,0]
	v_pk_fma_f32 v[98:99], v[98:99], v[98:99], s[22:23] neg_lo:[1,0,0] neg_hi:[1,0,0]
	v_pk_fma_f32 v[100:101], v[100:101], v[100:101], s[22:23] neg_lo:[1,0,0] neg_hi:[1,0,0]
	v_exp_f32_e32 v96, v96
	v_exp_f32_e32 v97, v97
	v_exp_f32_e32 v98, v98
	v_exp_f32_e32 v99, v99
	v_exp_f32_e32 v100, v100
	v_exp_f32_e32 v101, v101
	v_sub_f32_e32 v108, v18, v17
	v_sub_f32_e32 v104, v19, v18
	v_sub_f32_e32 v110, v20, v19
	v_sub_f32_e32 v106, v21, v20
	v_sub_f32_e64 v105, v22, v21
	v_fma_f32 v108, -v108, v108, s20
	v_fma_f32 v104, -v104, v104, s20
	v_fma_f32 v110, -v110, v110, s20
	v_fma_f32 v106, -v106, v106, s20
	v_fma_f32 v105, -v105, v105, s20
	v_exp_f32_e32 v108, v108
	v_exp_f32_e32 v104, v104
	v_exp_f32_e32 v110, v110
	v_exp_f32_e32 v106, v106
	v_exp_f32_e64 v105, v105
	v_pk_add_f32 v[64:65], v[64:65], v[96:97]
	v_pk_fma_f32 v[68:69], v[96:97], v[16:17], v[68:69]
	v_pk_add_f32 v[66:67], v[66:67], v[98:99]
	v_pk_add_f32 v[64:65], v[64:65], v[98:99]
	v_pk_fma_f32 v[68:69], v[98:99], v[20:21], v[68:69]
	v_pk_fma_f32 v[70:71], v[98:99], v[18:19], v[70:71]
	v_pk_add_f32 v[66:67], v[66:67], v[100:101]
	v_pk_fma_f32 v[70:71], v[100:101], v[22:23], v[70:71]
	v_add_f32_e32 v64, v64, v108
	v_fmac_f32_e32 v68, v108, v17
	v_add_f32_e32 v65, v65, v110
	v_fmac_f32_e32 v69, v110, v20
	v_add_f32_e32 v66, v66, v110
	v_fmac_f32_e32 v70, v110, v19
	v_add_f32_e32 v67, v67, v105
	v_fmac_f32_e32 v71, v105, v22
	v_pk_add_f32 v[64:65], v[64:65], v[104:105] op_sel_hi:[1,0]
	v_pk_fma_f32 v[68:69], v[104:105], v[18:19], v[68:69] op_sel:[0,1,0] op_sel_hi:[0,0,1]
	v_pk_add_f32 v[66:67], v[66:67], v[106:107] op_sel_hi:[1,0]
	v_pk_fma_f32 v[70:71], v[106:107], v[20:21], v[70:71] op_sel:[0,1,0] op_sel_hi:[0,0,1]
	s_waitcnt vmcnt(18)
	s_nop 0
	v_mov_b32_dpp v24, v28 row_shr:1 row_mask:0xf bank_mask:0xf
	v_mov_b32_dpp v25, v29 row_shr:1 row_mask:0xf bank_mask:0xf
	v_mov_b32_dpp v30, v26 row_shl:1 row_mask:0xf bank_mask:0xf
	v_mov_b32_dpp v31, v27 row_shl:1 row_mask:0xf bank_mask:0xf
	v_pk_mul_f32 v[26:27], v[26:27], s[32:33]
	v_pk_mul_f32 v[28:29], v[28:29], s[32:33]
	v_cndmask_b32_e64 v25, v25, v24, vcc
	v_cndmask_b32_e64 v30, v30, v31, s[16:17]
	v_pk_mul_f32 v[76:77], v[26:27], s[30:31]
	v_pk_mul_f32 v[78:79], v[28:29], s[30:31]
	v_pk_mul_f32 v[24:25], v[24:25], s[32:33]
	v_pk_mul_f32 v[30:31], v[30:31], s[32:33]
	v_mov_b32_e32 v72, s30
	v_mov_b32_e32 v73, s30
	v_mov_b32_e64 v74, s30
	v_mov_b32_e32 v75, s30
	s_setprio 3
	v_pk_add_f32 v[96:97], v[26:27], v[16:17] neg_lo:[0,1] neg_hi:[0,1]
	v_pk_add_f32 v[98:99], v[24:25], v[18:19] neg_lo:[0,1] neg_hi:[0,1]
	v_pk_add_f32 v[100:101], v[26:27], v[18:19] neg_lo:[0,1] neg_hi:[0,1]
	v_pk_add_f32 v[102:103], v[28:29], v[18:19] neg_lo:[0,1] neg_hi:[0,1]
	v_pk_fma_f32 v[96:97], v[96:97], v[96:97], s[26:27] neg_lo:[1,0,0] neg_hi:[1,0,0]
	v_pk_fma_f32 v[98:99], v[98:99], v[98:99], s[26:27] neg_lo:[1,0,0] neg_hi:[1,0,0]
	v_pk_fma_f32 v[100:101], v[100:101], v[100:101], s[20:21] neg_lo:[1,0,0] neg_hi:[1,0,0]
	v_pk_fma_f32 v[102:103], v[102:103], v[102:103], s[26:27] neg_lo:[1,0,0] neg_hi:[1,0,0]
	v_exp_f32_e32 v96, v96
	v_exp_f32_e32 v97, v97
	v_exp_f32_e32 v98, v98
	v_exp_f32_e32 v99, v99
	v_exp_f32_e32 v100, v100
	v_exp_f32_e32 v101, v101
	v_exp_f32_e32 v102, v102
	v_exp_f32_e32 v103, v103
	v_pk_add_f32 v[104:105], v[26:27], v[20:21] neg_lo:[0,1] neg_hi:[0,1]
	v_pk_add_f32 v[106:107], v[28:29], v[20:21] neg_lo:[0,1] neg_hi:[0,1]
	v_pk_add_f32 v[108:109], v[30:31], v[20:21] neg_lo:[0,1] neg_hi:[0,1]
	v_pk_add_f32 v[110:111], v[28:29], v[22:23] neg_lo:[0,1] neg_hi:[0,1]
	v_pk_fma_f32 v[104:105], v[104:105], v[104:105], s[26:27] neg_lo:[1,0,0] neg_hi:[1,0,0]
	v_pk_fma_f32 v[106:107], v[106:107], v[106:107], s[20:21] neg_lo:[1,0,0] neg_hi:[1,0,0]
	v_pk_fma_f32 v[108:109], v[108:109], v[108:109], s[26:27] neg_lo:[1,0,0] neg_hi:[1,0,0]
	v_pk_fma_f32 v[110:111], v[110:111], v[110:111], s[26:27] neg_lo:[1,0,0] neg_hi:[1,0,0]
	v_exp_f32_e32 v104, v104
	v_exp_f32_e32 v105, v105
	v_exp_f32_e32 v106, v106
	v_exp_f32_e32 v107, v107
	v_exp_f32_e32 v108, v108
	v_exp_f32_e32 v109, v109
	v_exp_f32_e32 v110, v110
	v_exp_f32_e32 v111, v111
	v_pk_add_f32 v[72:73], v[72:73], v[96:97]
	v_pk_fma_f32 v[76:77], v[96:97], v[16:17], v[76:77]
	v_pk_add_f32 v[64:65], v[64:65], v[98:99]
	v_pk_fma_f32 v[68:69], v[98:99], v[24:25], v[68:69]
	v_pk_add_f32 v[72:73], v[72:73], v[100:101]
	v_pk_add_f32 v[64:65], v[64:65], v[100:101]
	v_pk_fma_f32 v[68:69], v[100:101], v[26:27], v[68:69]
	v_pk_fma_f32 v[76:77], v[100:101], v[18:19], v[76:77]
	v_pk_add_f32 v[64:65], v[64:65], v[102:103]
	v_pk_fma_f32 v[68:69], v[102:103], v[28:29], v[68:69]
	v_pk_add_f32 v[74:75], v[74:75], v[102:103]
	v_pk_fma_f32 v[78:79], v[102:103], v[18:19], v[78:79]
	v_pk_add_f32 v[96:97], v[26:27], v[18:19] op_sel:[1,0] op_sel_hi:[0,1] neg_lo:[0,1] neg_hi:[0,1]
	v_pk_add_f32 v[98:99], v[28:29], v[20:21] op_sel:[1,0] op_sel_hi:[0,1] neg_lo:[0,1] neg_hi:[0,1]
	v_pk_add_f32 v[100:101], v[26:27], v[24:25] neg_lo:[0,1] neg_hi:[0,1]
	v_pk_add_f32 v[102:103], v[28:29], v[26:27] neg_lo:[0,1] neg_hi:[0,1]
	v_pk_fma_f32 v[96:97], v[96:97], v[96:97], s[24:25] neg_lo:[1,0,0] neg_hi:[1,0,0]
	v_pk_fma_f32 v[98:99], v[98:99], v[98:99], s[24:25] neg_lo:[1,0,0] neg_hi:[1,0,0]
	v_pk_fma_f32 v[100:101], v[100:101], v[100:101], s[22:23] neg_lo:[1,0,0] neg_hi:[1,0,0]
	v_pk_fma_f32 v[102:103], v[102:103], v[102:103], s[22:23] neg_lo:[1,0,0] neg_hi:[1,0,0]
	v_exp_f32_e32 v96, v96
	v_exp_f32_e32 v97, v97
	v_exp_f32_e32 v98, v98
	v_exp_f32_e32 v99, v99
	v_exp_f32_e32 v100, v100
	v_exp_f32_e32 v101, v101
	v_exp_f32_e32 v102, v102
	v_exp_f32_e32 v103, v103
	v_pk_add_f32 v[66:67], v[66:67], v[104:105]
	v_pk_fma_f32 v[70:71], v[104:105], v[26:27], v[70:71]
	v_pk_add_f32 v[72:73], v[72:73], v[104:105]
	v_pk_fma_f32 v[76:77], v[104:105], v[20:21], v[76:77]
	v_pk_add_f32 v[66:67], v[66:67], v[106:107]
	v_pk_fma_f32 v[70:71], v[106:107], v[28:29], v[70:71]
	v_pk_add_f32 v[74:75], v[74:75], v[106:107]
	v_pk_fma_f32 v[78:79], v[106:107], v[20:21], v[78:79]
	v_pk_add_f32 v[66:67], v[66:67], v[108:109]
	v_pk_fma_f32 v[70:71], v[108:109], v[30:31], v[70:71]
	v_pk_add_f32 v[74:75], v[74:75], v[110:111]
	v_pk_fma_f32 v[78:79], v[110:111], v[22:23], v[78:79]
	v_pk_add_f32 v[104:105], v[30:31], v[28:29] neg_lo:[0,1] neg_hi:[0,1]
	v_pk_fma_f32 v[104:105], v[104:105], v[104:105], s[22:23] neg_lo:[1,0,0] neg_hi:[1,0,0]
	s_nop 0
	v_exp_f32_e32 v104, v104
	v_exp_f32_e64 v105, v105
	v_pk_add_f32 v[64:65], v[64:65], v[96:97]
	v_pk_fma_f32 v[68:69], v[96:97], v[26:27], v[68:69] op_sel:[0,1,0] op_sel_hi:[1,0,1]
	v_pk_add_f32 v[72:73], v[72:73], v[96:97] op_sel:[0,1] op_sel_hi:[1,0]
	v_pk_fma_f32 v[76:77], v[96:97], v[18:19], v[76:77] op_sel:[1,1,0] op_sel_hi:[0,0,1]
	v_pk_add_f32 v[66:67], v[66:67], v[98:99]
	v_pk_fma_f32 v[70:71], v[98:99], v[28:29], v[70:71] op_sel:[0,1,0] op_sel_hi:[1,0,1]
	v_pk_add_f32 v[74:75], v[74:75], v[98:99] op_sel:[0,1] op_sel_hi:[1,0]
	v_pk_fma_f32 v[78:79], v[98:99], v[20:21], v[78:79] op_sel:[1,1,0] op_sel_hi:[0,0,1]
	v_pk_add_f32 v[72:73], v[72:73], v[100:101]
	v_pk_fma_f32 v[76:77], v[100:101], v[24:25], v[76:77]
	v_pk_add_f32 v[74:75], v[74:75], v[102:103]
	v_pk_add_f32 v[72:73], v[72:73], v[102:103]
	v_pk_fma_f32 v[76:77], v[102:103], v[28:29], v[76:77]
	v_pk_fma_f32 v[78:79], v[102:103], v[26:27], v[78:79]
	s_nop 0
	v_sub_f32_e32 v98, v26, v17
	v_sub_f32_e32 v100, v25, v18
	v_sub_f32_e32 v102, v28, v19
	v_sub_f32_e32 v97, v27, v20
	v_sub_f32_e32 v99, v30, v21
	v_sub_f32_e32 v101, v29, v22
	v_sub_f32_e32 v103, v26, v25
	v_sub_f32_e64 v96, v27, v26
	v_fma_f32 v98, -v98, v98, s24
	v_fma_f32 v100, -v100, v100, s24
	v_fma_f32 v102, -v102, v102, s24
	v_fma_f32 v97, -v97, v97, s24
	v_fma_f32 v99, -v99, v99, s24
	v_fma_f32 v101, -v101, v101, s24
	v_fma_f32 v103, -v103, v103, s20
	v_fma_f32 v96, -v96, v96, s20
	v_exp_f32_e32 v98, v98
	v_exp_f32_e32 v100, v100
	v_exp_f32_e32 v102, v102
	v_exp_f32_e32 v97, v97
	v_exp_f32_e32 v99, v99
	v_exp_f32_e32 v101, v101
	v_exp_f32_e32 v103, v103
	v_exp_f32_e32 v96, v96
	v_pk_add_f32 v[74:75], v[74:75], v[104:105]
	v_pk_fma_f32 v[78:79], v[104:105], v[30:31], v[78:79]
	v_sub_f32_e32 v106, v28, v27
	v_sub_f32_e32 v104, v29, v28
	v_sub_f32_e64 v108, v30, v29
	v_fma_f32 v106, -v106, v106, s20
	v_fma_f32 v104, -v104, v104, s20
	v_fma_f32 v108, -v108, v108, s20
	v_exp_f32_e32 v106, v106
	v_exp_f32_e32 v104, v104
	v_exp_f32_e32 v108, v108
	v_add_f32_e32 v72, v72, v98
	v_fmac_f32_e32 v76, v98, v17
	v_add_f32_e32 v64, v64, v100
	v_fmac_f32_e32 v68, v100, v25
	v_add_f32_e32 v65, v65, v102
	v_fmac_f32_e32 v69, v102, v28
	v_add_f32_e32 v74, v74, v102
	v_fmac_f32_e32 v78, v102, v19
	v_add_f32_e32 v66, v66, v97
	v_fmac_f32_e32 v70, v97, v27
	v_add_f32_e32 v73, v73, v97
	v_fmac_f32_e32 v77, v97, v20
	v_add_f32_e32 v67, v67, v99
	v_fmac_f32_e32 v71, v99, v30
	v_add_f32_e32 v75, v75, v101
	v_fmac_f32_e32 v79, v101, v22
	v_add_f32_e32 v72, v72, v103
	v_fmac_f32_e64 v76, v103, v25
	v_pk_add_f32 v[72:73], v[72:73], v[96:97] op_sel_hi:[1,0]
	v_pk_fma_f32 v[76:77], v[96:97], v[26:27], v[76:77] op_sel:[0,1,0] op_sel_hi:[0,0,1]
	v_add_f32_e32 v73, v73, v106
	v_fmac_f32_e32 v77, v106, v28
	v_add_f32_e32 v74, v74, v106
	v_fmac_f32_e32 v78, v106, v27
	v_add_f32_e32 v75, v75, v108
	v_fmac_f32_e32 v79, v108, v30
	v_pk_add_f32 v[74:75], v[74:75], v[104:105] op_sel_hi:[1,0]
	v_pk_fma_f32 v[78:79], v[104:105], v[28:29], v[78:79] op_sel:[0,1,0] op_sel_hi:[0,0,1]
	s_waitcnt vmcnt(15)
	s_nop 0
	v_mov_b32_dpp v8, v12 row_shr:1 row_mask:0xf bank_mask:0xf
	v_mov_b32_dpp v9, v13 row_shr:1 row_mask:0xf bank_mask:0xf
	v_mov_b32_dpp v14, v10 row_shl:1 row_mask:0xf bank_mask:0xf
	v_mov_b32_dpp v15, v11 row_shl:1 row_mask:0xf bank_mask:0xf
	v_pk_mul_f32 v[10:11], v[10:11], s[32:33]
	v_pk_mul_f32 v[12:13], v[12:13], s[32:33]
	v_cndmask_b32_e64 v9, v9, v8, vcc
	v_cndmask_b32_e64 v14, v14, v15, s[16:17]
	v_pk_mul_f32 v[8:9], v[8:9], s[32:33]
	v_pk_mul_f32 v[14:15], v[14:15], s[32:33]
	s_setprio 3
	s_nop 0
	v_pk_add_f32 v[96:97], v[18:19], v[8:9] neg_lo:[0,1] neg_hi:[0,1]
	v_pk_add_f32 v[98:99], v[18:19], v[10:11] neg_lo:[0,1] neg_hi:[0,1]
	v_pk_add_f32 v[100:101], v[20:21], v[10:11] neg_lo:[0,1] neg_hi:[0,1]
	v_pk_add_f32 v[102:103], v[18:19], v[12:13] neg_lo:[0,1] neg_hi:[0,1]
	v_pk_fma_f32 v[96:97], v[96:97], v[96:97], s[26:27] neg_lo:[1,0,0] neg_hi:[1,0,0]
	v_pk_fma_f32 v[98:99], v[98:99], v[98:99], s[20:21] neg_lo:[1,0,0] neg_hi:[1,0,0]
	v_pk_fma_f32 v[100:101], v[100:101], v[100:101], s[26:27] neg_lo:[1,0,0] neg_hi:[1,0,0]
	v_pk_fma_f32 v[102:103], v[102:103], v[102:103], s[26:27] neg_lo:[1,0,0] neg_hi:[1,0,0]
	v_exp_f32_e32 v96, v96
	v_exp_f32_e32 v97, v97
	v_exp_f32_e32 v98, v98
	v_exp_f32_e32 v99, v99
	v_exp_f32_e32 v100, v100
	v_exp_f32_e32 v101, v101
	v_exp_f32_e32 v102, v102
	v_exp_f32_e32 v103, v103
	v_pk_add_f32 v[104:105], v[20:21], v[12:13] neg_lo:[0,1] neg_hi:[0,1]
	v_pk_add_f32 v[106:107], v[20:21], v[14:15] neg_lo:[0,1] neg_hi:[0,1]
	v_pk_add_f32 v[108:109], v[18:19], v[10:11] op_sel:[1,0] op_sel_hi:[0,1] neg_lo:[0,1] neg_hi:[0,1]
	v_pk_add_f32 v[110:111], v[20:21], v[12:13] op_sel:[1,0] op_sel_hi:[0,1] neg_lo:[0,1] neg_hi:[0,1]
	v_pk_fma_f32 v[104:105], v[104:105], v[104:105], s[20:21] neg_lo:[1,0,0] neg_hi:[1,0,0]
	v_pk_fma_f32 v[106:107], v[106:107], v[106:107], s[26:27] neg_lo:[1,0,0] neg_hi:[1,0,0]
	v_pk_fma_f32 v[108:109], v[108:109], v[108:109], s[24:25] neg_lo:[1,0,0] neg_hi:[1,0,0]
	v_pk_fma_f32 v[110:111], v[110:111], v[110:111], s[24:25] neg_lo:[1,0,0] neg_hi:[1,0,0]
	v_exp_f32_e32 v104, v104
	v_exp_f32_e32 v105, v105
	v_exp_f32_e32 v106, v106
	v_exp_f32_e32 v107, v107
	v_exp_f32_e32 v108, v108
	v_exp_f32_e32 v109, v109
	v_exp_f32_e32 v110, v110
	v_exp_f32_e32 v111, v111
	v_pk_add_f32 v[64:65], v[64:65], v[96:97]
	v_pk_fma_f32 v[68:69], v[96:97], v[8:9], v[68:69]
	v_pk_add_f32 v[66:67], v[66:67], v[100:101]
	v_pk_add_f32 v[64:65], v[64:65], v[98:99]
	v_pk_fma_f32 v[68:69], v[98:99], v[10:11], v[68:69]
	v_pk_fma_f32 v[70:71], v[100:101], v[10:11], v[70:71]
	v_pk_add_f32 v[64:65], v[64:65], v[102:103]
	v_pk_fma_f32 v[68:69], v[102:103], v[12:13], v[68:69]
	v_pk_add_f32 v[96:97], v[26:27], v[8:9] neg_lo:[0,1] neg_hi:[0,1]
	v_pk_add_f32 v[98:99], v[26:27], v[10:11] neg_lo:[0,1] neg_hi:[0,1]
	v_pk_add_f32 v[100:101], v[28:29], v[10:11] neg_lo:[0,1] neg_hi:[0,1]
	v_pk_add_f32 v[102:103], v[26:27], v[12:13] neg_lo:[0,1] neg_hi:[0,1]
	v_pk_fma_f32 v[96:97], v[96:97], v[96:97], s[28:29] neg_lo:[1,0,0] neg_hi:[1,0,0]
	v_pk_fma_f32 v[98:99], v[98:99], v[98:99], s[22:23] neg_lo:[1,0,0] neg_hi:[1,0,0]
	v_pk_fma_f32 v[100:101], v[100:101], v[100:101], s[28:29] neg_lo:[1,0,0] neg_hi:[1,0,0]
	v_pk_fma_f32 v[102:103], v[102:103], v[102:103], s[28:29] neg_lo:[1,0,0] neg_hi:[1,0,0]
	v_exp_f32_e32 v96, v96
	v_exp_f32_e32 v97, v97
	v_exp_f32_e32 v98, v98
	v_exp_f32_e32 v99, v99
	v_exp_f32_e32 v100, v100
	v_exp_f32_e32 v101, v101
	v_exp_f32_e32 v102, v102
	v_exp_f32_e32 v103, v103
	v_pk_add_f32 v[66:67], v[66:67], v[104:105]
	v_pk_fma_f32 v[70:71], v[104:105], v[12:13], v[70:71]
	v_pk_add_f32 v[64:65], v[64:65], v[108:109] op_sel:[0,1] op_sel_hi:[1,0]
	v_pk_add_f32 v[66:67], v[66:67], v[106:107]
	v_pk_fma_f32 v[70:71], v[106:107], v[14:15], v[70:71]
	v_pk_fma_f32 v[68:69], v[108:109], v[10:11], v[68:69] op_sel:[1,1,0] op_sel_hi:[0,0,1]
	v_pk_add_f32 v[66:67], v[66:67], v[110:111] op_sel:[0,1] op_sel_hi:[1,0]
	v_pk_fma_f32 v[70:71], v[110:111], v[12:13], v[70:71] op_sel:[1,1,0] op_sel_hi:[0,0,1]
	v_pk_add_f32 v[104:105], v[28:29], v[12:13] neg_lo:[0,1] neg_hi:[0,1]
	v_pk_add_f32 v[106:107], v[28:29], v[14:15] neg_lo:[0,1] neg_hi:[0,1]
	v_pk_add_f32 v[108:109], v[26:27], v[10:11] op_sel:[1,0] op_sel_hi:[0,1] neg_lo:[0,1] neg_hi:[0,1]
	v_pk_add_f32 v[110:111], v[28:29], v[12:13] op_sel:[1,0] op_sel_hi:[0,1] neg_lo:[0,1] neg_hi:[0,1]
	v_pk_fma_f32 v[104:105], v[104:105], v[104:105], s[22:23] neg_lo:[1,0,0] neg_hi:[1,0,0]
	v_pk_fma_f32 v[106:107], v[106:107], v[106:107], s[28:29] neg_lo:[1,0,0] neg_hi:[1,0,0]
	v_pk_fma_f32 v[108:109], v[108:109], v[108:109], s[26:27] neg_lo:[1,0,0] neg_hi:[1,0,0]
	v_pk_fma_f32 v[110:111], v[110:111], v[110:111], s[26:27] neg_lo:[1,0,0] neg_hi:[1,0,0]
	v_exp_f32_e32 v104, v104
	v_exp_f32_e32 v105, v105
	v_exp_f32_e32 v106, v106
	v_exp_f32_e32 v107, v107
	v_exp_f32_e32 v108, v108
	v_exp_f32_e32 v109, v109
	v_exp_f32_e32 v110, v110
	v_exp_f32_e32 v111, v111
	v_pk_add_f32 v[72:73], v[72:73], v[96:97]
	v_pk_fma_f32 v[76:77], v[96:97], v[8:9], v[76:77]
	v_pk_add_f32 v[74:75], v[74:75], v[100:101]
	v_pk_add_f32 v[72:73], v[72:73], v[98:99]
	v_pk_fma_f32 v[76:77], v[98:99], v[10:11], v[76:77]
	v_pk_fma_f32 v[78:79], v[100:101], v[10:11], v[78:79]
	v_pk_add_f32 v[72:73], v[72:73], v[102:103]
	v_pk_fma_f32 v[76:77], v[102:103], v[12:13], v[76:77]
	v_sub_f32_e32 v96, v18, v9
	v_sub_f32_e32 v98, v20, v11
	v_sub_f32_e32 v100, v19, v12
	v_sub_f32_e32 v102, v21, v14
	v_sub_f32_e32 v97, v26, v9
	v_sub_f32_e32 v99, v28, v11
	v_sub_f32_e32 v101, v27, v12
	v_sub_f32_e32 v103, v29, v14
	v_fma_f32 v96, -v96, v96, s24
	v_fma_f32 v98, -v98, v98, s24
	v_fma_f32 v100, -v100, v100, s24
	v_fma_f32 v102, -v102, v102, s24
	v_fma_f32 v97, -v97, v97, s26
	v_fma_f32 v99, -v99, v99, s26
	v_fma_f32 v101, -v101, v101, s26
	v_fma_f32 v103, -v103, v103, s26
	v_exp_f32_e32 v96, v96
	v_exp_f32_e32 v98, v98
	v_exp_f32_e32 v100, v100
	v_exp_f32_e32 v102, v102
	v_exp_f32_e32 v97, v97
	v_exp_f32_e32 v99, v99
	v_exp_f32_e32 v101, v101
	v_exp_f32_e32 v103, v103
	v_pk_add_f32 v[74:75], v[74:75], v[104:105]
	v_pk_fma_f32 v[78:79], v[104:105], v[12:13], v[78:79]
	v_pk_add_f32 v[72:73], v[72:73], v[108:109] op_sel:[0,1] op_sel_hi:[1,0]
	v_pk_add_f32 v[74:75], v[74:75], v[106:107]
	v_pk_fma_f32 v[78:79], v[106:107], v[14:15], v[78:79]
	v_pk_fma_f32 v[76:77], v[108:109], v[10:11], v[76:77] op_sel:[1,1,0] op_sel_hi:[0,0,1]
	v_pk_add_f32 v[74:75], v[74:75], v[110:111] op_sel:[0,1] op_sel_hi:[1,0]
	v_pk_fma_f32 v[78:79], v[110:111], v[12:13], v[78:79] op_sel:[1,1,0] op_sel_hi:[0,0,1]
	v_add_f32_e32 v64, v64, v96
	v_fmac_f32_e32 v68, v96, v9
	v_add_f32_e32 v66, v66, v98
	v_fmac_f32_e32 v70, v98, v11
	v_add_f32_e32 v65, v65, v100
	v_fmac_f32_e32 v69, v100, v12
	v_add_f32_e32 v67, v67, v102
	v_fmac_f32_e32 v71, v102, v14
	v_add_f32_e32 v72, v72, v97
	v_fmac_f32_e32 v76, v97, v9
	v_add_f32_e32 v74, v74, v99
	v_fmac_f32_e32 v78, v99, v11
	v_add_f32_e32 v73, v73, v101
	v_fmac_f32_e32 v77, v101, v12
	v_add_f32_e64 v75, v75, v103
	v_fmac_f32_e32 v79, v103, v14
	s_waitcnt vmcnt(12)
	v_mov_b32_dpp v32, v36 row_shr:1 row_mask:0xf bank_mask:0xf
	v_mov_b32_dpp v33, v37 row_shr:1 row_mask:0xf bank_mask:0xf
	v_mov_b32_dpp v38, v34 row_shl:1 row_mask:0xf bank_mask:0xf
	v_mov_b32_dpp v39, v35 row_shl:1 row_mask:0xf bank_mask:0xf
	v_pk_mul_f32 v[34:35], v[34:35], s[32:33]
	v_pk_mul_f32 v[36:37], v[36:37], s[32:33]
	v_cndmask_b32_e64 v33, v33, v32, vcc
	v_cndmask_b32_e64 v38, v38, v39, s[16:17]
	v_pk_mul_f32 v[84:85], v[34:35], s[30:31]
	v_pk_mul_f32 v[86:87], v[36:37], s[30:31]
	v_pk_mul_f32 v[32:33], v[32:33], s[32:33]
	v_pk_mul_f32 v[38:39], v[38:39], s[32:33]
	v_mov_b32_e32 v80, s30
	v_mov_b32_e32 v81, s30
	v_mov_b32_e64 v82, s30
	v_mov_b32_e32 v83, s30
	s_setprio 2
	v_pk_add_f32 v[96:97], v[34:35], v[16:17] neg_lo:[0,1] neg_hi:[0,1]
	v_pk_add_f32 v[98:99], v[32:33], v[18:19] neg_lo:[0,1] neg_hi:[0,1]
	v_pk_add_f32 v[100:101], v[34:35], v[18:19] neg_lo:[0,1] neg_hi:[0,1]
	v_pk_add_f32 v[102:103], v[36:37], v[18:19] neg_lo:[0,1] neg_hi:[0,1]
	v_pk_fma_f32 v[96:97], v[96:97], v[96:97], s[28:29] neg_lo:[1,0,0] neg_hi:[1,0,0]
	v_pk_fma_f32 v[98:99], v[98:99], v[98:99], s[28:29] neg_lo:[1,0,0] neg_hi:[1,0,0]
	v_pk_fma_f32 v[100:101], v[100:101], v[100:101], s[22:23] neg_lo:[1,0,0] neg_hi:[1,0,0]
	v_pk_fma_f32 v[102:103], v[102:103], v[102:103], s[28:29] neg_lo:[1,0,0] neg_hi:[1,0,0]
	v_exp_f32_e32 v96, v96
	v_exp_f32_e32 v97, v97
	v_exp_f32_e32 v98, v98
	v_exp_f32_e32 v99, v99
	v_exp_f32_e32 v100, v100
	v_exp_f32_e32 v101, v101
	v_exp_f32_e32 v102, v102
	v_exp_f32_e32 v103, v103
	v_pk_add_f32 v[104:105], v[34:35], v[20:21] neg_lo:[0,1] neg_hi:[0,1]
	v_pk_add_f32 v[106:107], v[36:37], v[20:21] neg_lo:[0,1] neg_hi:[0,1]
	v_pk_add_f32 v[108:109], v[38:39], v[20:21] neg_lo:[0,1] neg_hi:[0,1]
	v_pk_add_f32 v[110:111], v[36:37], v[22:23] neg_lo:[0,1] neg_hi:[0,1]
	v_pk_fma_f32 v[104:105], v[104:105], v[104:105], s[28:29] neg_lo:[1,0,0] neg_hi:[1,0,0]
	v_pk_fma_f32 v[106:107], v[106:107], v[106:107], s[22:23] neg_lo:[1,0,0] neg_hi:[1,0,0]
	v_pk_fma_f32 v[108:109], v[108:109], v[108:109], s[28:29] neg_lo:[1,0,0] neg_hi:[1,0,0]
	v_pk_fma_f32 v[110:111], v[110:111], v[110:111], s[28:29] neg_lo:[1,0,0] neg_hi:[1,0,0]
	v_exp_f32_e32 v104, v104
	v_exp_f32_e32 v105, v105
	v_exp_f32_e32 v106, v106
	v_exp_f32_e32 v107, v107
	v_exp_f32_e32 v108, v108
	v_exp_f32_e32 v109, v109
	v_exp_f32_e32 v110, v110
	v_exp_f32_e32 v111, v111
	v_pk_add_f32 v[80:81], v[80:81], v[96:97]
	v_pk_fma_f32 v[84:85], v[96:97], v[16:17], v[84:85]
	v_pk_add_f32 v[64:65], v[64:65], v[98:99]
	v_pk_fma_f32 v[68:69], v[98:99], v[32:33], v[68:69]
	v_pk_add_f32 v[80:81], v[80:81], v[100:101]
	v_pk_add_f32 v[64:65], v[64:65], v[100:101]
	v_pk_fma_f32 v[68:69], v[100:101], v[34:35], v[68:69]
	v_pk_fma_f32 v[84:85], v[100:101], v[18:19], v[84:85]
	v_pk_add_f32 v[64:65], v[64:65], v[102:103]
	v_pk_fma_f32 v[68:69], v[102:103], v[36:37], v[68:69]
	v_pk_add_f32 v[82:83], v[82:83], v[102:103]
	v_pk_fma_f32 v[86:87], v[102:103], v[18:19], v[86:87]
	v_pk_add_f32 v[96:97], v[34:35], v[18:19] op_sel:[1,0] op_sel_hi:[0,1] neg_lo:[0,1] neg_hi:[0,1]
	v_pk_add_f32 v[98:99], v[36:37], v[20:21] op_sel:[1,0] op_sel_hi:[0,1] neg_lo:[0,1] neg_hi:[0,1]
	v_pk_add_f32 v[100:101], v[34:35], v[24:25] neg_lo:[0,1] neg_hi:[0,1]
	v_pk_add_f32 v[102:103], v[32:33], v[26:27] neg_lo:[0,1] neg_hi:[0,1]
	v_pk_fma_f32 v[96:97], v[96:97], v[96:97], s[26:27] neg_lo:[1,0,0] neg_hi:[1,0,0]
	v_pk_fma_f32 v[98:99], v[98:99], v[98:99], s[26:27] neg_lo:[1,0,0] neg_hi:[1,0,0]
	v_pk_fma_f32 v[100:101], v[100:101], v[100:101], s[26:27] neg_lo:[1,0,0] neg_hi:[1,0,0]
	v_pk_fma_f32 v[102:103], v[102:103], v[102:103], s[26:27] neg_lo:[1,0,0] neg_hi:[1,0,0]
	v_exp_f32_e32 v96, v96
	v_exp_f32_e32 v97, v97
	v_exp_f32_e32 v98, v98
	v_exp_f32_e32 v99, v99
	v_exp_f32_e32 v100, v100
	v_exp_f32_e32 v101, v101
	v_exp_f32_e32 v102, v102
	v_exp_f32_e32 v103, v103
	v_pk_add_f32 v[66:67], v[66:67], v[104:105]
	v_pk_fma_f32 v[70:71], v[104:105], v[34:35], v[70:71]
	v_pk_add_f32 v[80:81], v[80:81], v[104:105]
	v_pk_fma_f32 v[84:85], v[104:105], v[20:21], v[84:85]
	v_pk_add_f32 v[66:67], v[66:67], v[106:107]
	v_pk_fma_f32 v[70:71], v[106:107], v[36:37], v[70:71]
	v_pk_add_f32 v[82:83], v[82:83], v[106:107]
	v_pk_fma_f32 v[86:87], v[106:107], v[20:21], v[86:87]
	v_pk_add_f32 v[66:67], v[66:67], v[108:109]
	v_pk_fma_f32 v[70:71], v[108:109], v[38:39], v[70:71]
	v_pk_add_f32 v[82:83], v[82:83], v[110:111]
	v_pk_fma_f32 v[86:87], v[110:111], v[22:23], v[86:87]
	v_pk_add_f32 v[104:105], v[34:35], v[26:27] neg_lo:[0,1] neg_hi:[0,1]
	v_pk_add_f32 v[106:107], v[36:37], v[26:27] neg_lo:[0,1] neg_hi:[0,1]
	v_pk_add_f32 v[108:109], v[34:35], v[28:29] neg_lo:[0,1] neg_hi:[0,1]
	v_pk_add_f32 v[110:111], v[36:37], v[28:29] neg_lo:[0,1] neg_hi:[0,1]
	v_pk_fma_f32 v[104:105], v[104:105], v[104:105], s[20:21] neg_lo:[1,0,0] neg_hi:[1,0,0]
	v_pk_fma_f32 v[106:107], v[106:107], v[106:107], s[26:27] neg_lo:[1,0,0] neg_hi:[1,0,0]
	v_pk_fma_f32 v[108:109], v[108:109], v[108:109], s[26:27] neg_lo:[1,0,0] neg_hi:[1,0,0]
	v_pk_fma_f32 v[110:111], v[110:111], v[110:111], s[20:21] neg_lo:[1,0,0] neg_hi:[1,0,0]
	v_exp_f32_e32 v104, v104
	v_exp_f32_e32 v105, v105
	v_exp_f32_e32 v106, v106
	v_exp_f32_e32 v107, v107
	v_exp_f32_e32 v108, v108
	v_exp_f32_e32 v109, v109
	v_exp_f32_e32 v110, v110
	v_exp_f32_e32 v111, v111
	v_pk_add_f32 v[64:65], v[64:65], v[96:97]
	v_pk_fma_f32 v[68:69], v[96:97], v[34:35], v[68:69] op_sel:[0,1,0] op_sel_hi:[1,0,1]
	v_pk_add_f32 v[80:81], v[80:81], v[96:97] op_sel:[0,1] op_sel_hi:[1,0]
	v_pk_fma_f32 v[84:85], v[96:97], v[18:19], v[84:85] op_sel:[1,1,0] op_sel_hi:[0,0,1]
	v_pk_add_f32 v[66:67], v[66:67], v[98:99]
	v_pk_fma_f32 v[70:71], v[98:99], v[36:37], v[70:71] op_sel:[0,1,0] op_sel_hi:[1,0,1]
	v_pk_add_f32 v[82:83], v[82:83], v[98:99] op_sel:[0,1] op_sel_hi:[1,0]
	v_pk_fma_f32 v[86:87], v[98:99], v[20:21], v[86:87] op_sel:[1,1,0] op_sel_hi:[0,0,1]
	v_pk_add_f32 v[80:81], v[80:81], v[100:101]
	v_pk_fma_f32 v[84:85], v[100:101], v[24:25], v[84:85]
	v_pk_add_f32 v[72:73], v[72:73], v[102:103]
	v_pk_fma_f32 v[76:77], v[102:103], v[32:33], v[76:77]
	v_pk_add_f32 v[96:97], v[38:39], v[28:29] neg_lo:[0,1] neg_hi:[0,1]
	v_pk_add_f32 v[98:99], v[36:37], v[30:31] neg_lo:[0,1] neg_hi:[0,1]
	v_pk_add_f32 v[100:101], v[34:35], v[26:27] op_sel:[1,0] op_sel_hi:[0,1] neg_lo:[0,1] neg_hi:[0,1]
	v_pk_add_f32 v[102:103], v[36:37], v[28:29] op_sel:[1,0] op_sel_hi:[0,1] neg_lo:[0,1] neg_hi:[0,1]
	v_pk_fma_f32 v[96:97], v[96:97], v[96:97], s[26:27] neg_lo:[1,0,0] neg_hi:[1,0,0]
	v_pk_fma_f32 v[98:99], v[98:99], v[98:99], s[26:27] neg_lo:[1,0,0] neg_hi:[1,0,0]
	v_pk_fma_f32 v[100:101], v[100:101], v[100:101], s[24:25] neg_lo:[1,0,0] neg_hi:[1,0,0]
	v_pk_fma_f32 v[102:103], v[102:103], v[102:103], s[24:25] neg_lo:[1,0,0] neg_hi:[1,0,0]
	v_exp_f32_e32 v96, v96
	v_exp_f32_e32 v97, v97
	v_exp_f32_e32 v98, v98
	v_exp_f32_e32 v99, v99
	v_exp_f32_e32 v100, v100
	v_exp_f32_e32 v101, v101
	v_exp_f32_e32 v102, v102
	v_exp_f32_e32 v103, v103
	v_pk_add_f32 v[72:73], v[72:73], v[104:105]
	v_pk_fma_f32 v[76:77], v[104:105], v[34:35], v[76:77]
	v_pk_add_f32 v[80:81], v[80:81], v[104:105]
	v_pk_fma_f32 v[84:85], v[104:105], v[26:27], v[84:85]
	v_pk_add_f32 v[72:73], v[72:73], v[106:107]
	v_pk_fma_f32 v[76:77], v[106:107], v[36:37], v[76:77]
	v_pk_add_f32 v[82:83], v[82:83], v[106:107]
	v_pk_fma_f32 v[86:87], v[106:107], v[26:27], v[86:87]
	v_pk_add_f32 v[74:75], v[74:75], v[108:109]
	v_pk_fma_f32 v[78:79], v[108:109], v[34:35], v[78:79]
	v_pk_add_f32 v[80:81], v[80:81], v[108:109]
	v_pk_fma_f32 v[84:85], v[108:109], v[28:29], v[84:85]
	v_pk_add_f32 v[74:75], v[74:75], v[110:111]
	v_pk_fma_f32 v[78:79], v[110:111], v[36:37], v[78:79]
	v_pk_add_f32 v[82:83], v[82:83], v[110:111]
	v_pk_fma_f32 v[86:87], v[110:111], v[28:29], v[86:87]
	v_pk_add_f32 v[104:105], v[34:35], v[32:33] neg_lo:[0,1] neg_hi:[0,1]
	v_pk_add_f32 v[106:107], v[36:37], v[34:35] neg_lo:[0,1] neg_hi:[0,1]
	v_pk_add_f32 v[108:109], v[38:39], v[36:37] neg_lo:[0,1] neg_hi:[0,1]
	v_pk_fma_f32 v[104:105], v[104:105], v[104:105], s[22:23] neg_lo:[1,0,0] neg_hi:[1,0,0]
	v_pk_fma_f32 v[106:107], v[106:107], v[106:107], s[22:23] neg_lo:[1,0,0] neg_hi:[1,0,0]
	v_pk_fma_f32 v[108:109], v[108:109], v[108:109], s[22:23] neg_lo:[1,0,0] neg_hi:[1,0,0]
	v_exp_f32_e32 v104, v104
	v_exp_f32_e32 v105, v105
	v_exp_f32_e32 v106, v106
	v_exp_f32_e32 v107, v107
	v_exp_f32_e32 v108, v108
	v_exp_f32_e32 v109, v109
	v_pk_add_f32 v[74:75], v[74:75], v[96:97]
	v_pk_fma_f32 v[78:79], v[96:97], v[38:39], v[78:79]
	v_pk_add_f32 v[82:83], v[82:83], v[98:99]
	v_pk_fma_f32 v[86:87], v[98:99], v[30:31], v[86:87]
	v_pk_add_f32 v[72:73], v[72:73], v[100:101]
	v_pk_fma_f32 v[76:77], v[100:101], v[34:35], v[76:77] op_sel:[0,1,0] op_sel_hi:[1,0,1]
	v_pk_add_f32 v[80:81], v[80:81], v[100:101] op_sel:[0,1] op_sel_hi:[1,0]
	v_pk_fma_f32 v[84:85], v[100:101], v[26:27], v[84:85] op_sel:[1,1,0] op_sel_hi:[0,0,1]
	v_pk_add_f32 v[74:75], v[74:75], v[102:103]
	v_pk_fma_f32 v[78:79], v[102:103], v[36:37], v[78:79] op_sel:[0,1,0] op_sel_hi:[1,0,1]
	v_pk_add_f32 v[82:83], v[82:83], v[102:103] op_sel:[0,1] op_sel_hi:[1,0]
	v_pk_fma_f32 v[86:87], v[102:103], v[28:29], v[86:87] op_sel:[1,1,0] op_sel_hi:[0,0,1]
	v_sub_f32_e32 v96, v34, v17
	v_sub_f32_e32 v98, v33, v18
	v_sub_f32_e32 v100, v36, v19
	v_sub_f32_e32 v102, v35, v20
	v_sub_f32_e32 v97, v38, v21
	v_sub_f32_e32 v99, v37, v22
	v_sub_f32_e32 v101, v34, v25
	v_sub_f32_e32 v103, v33, v26
	v_fma_f32 v96, -v96, v96, s26
	v_fma_f32 v98, -v98, v98, s26
	v_fma_f32 v100, -v100, v100, s26
	v_fma_f32 v102, -v102, v102, s26
	v_fma_f32 v97, -v97, v97, s26
	v_fma_f32 v99, -v99, v99, s26
	v_fma_f32 v101, -v101, v101, s24
	v_fma_f32 v103, -v103, v103, s24
	v_exp_f32_e32 v96, v96
	v_exp_f32_e32 v98, v98
	v_exp_f32_e32 v100, v100
	v_exp_f32_e32 v102, v102
	v_exp_f32_e32 v97, v97
	v_exp_f32_e32 v99, v99
	v_exp_f32_e32 v101, v101
	v_exp_f32_e32 v103, v103
	v_pk_add_f32 v[80:81], v[80:81], v[104:105]
	v_pk_fma_f32 v[84:85], v[104:105], v[32:33], v[84:85]
	v_pk_add_f32 v[82:83], v[82:83], v[106:107]
	v_pk_add_f32 v[80:81], v[80:81], v[106:107]
	v_pk_fma_f32 v[84:85], v[106:107], v[36:37], v[84:85]
	v_pk_fma_f32 v[86:87], v[106:107], v[34:35], v[86:87]
	v_pk_add_f32 v[82:83], v[82:83], v[108:109]
	v_pk_fma_f32 v[86:87], v[108:109], v[38:39], v[86:87]
	v_sub_f32_e32 v108, v36, v27
	v_sub_f32_e32 v110, v35, v28
	v_sub_f32_e32 v105, v38, v29
	v_sub_f32_e32 v107, v37, v30
	v_sub_f32_e32 v109, v34, v33
	v_sub_f32_e32 v104, v35, v34
	v_sub_f32_e32 v111, v36, v35
	v_sub_f32_e32 v106, v37, v36
	v_fma_f32 v108, -v108, v108, s24
	v_fma_f32 v110, -v110, v110, s24
	v_fma_f32 v105, -v105, v105, s24
	v_fma_f32 v107, -v107, v107, s24
	v_fma_f32 v109, -v109, v109, s20
	v_fma_f32 v104, -v104, v104, s20
	v_fma_f32 v111, -v111, v111, s20
	v_fma_f32 v106, -v106, v106, s20
	v_exp_f32_e32 v108, v108
	v_exp_f32_e32 v110, v110
	v_exp_f32_e32 v105, v105
	v_exp_f32_e32 v107, v107
	v_exp_f32_e32 v109, v109
	v_exp_f32_e32 v104, v104
	v_exp_f32_e32 v111, v111
	v_exp_f32_e32 v106, v106
	v_add_f32_e32 v80, v80, v96
	v_fmac_f32_e32 v84, v96, v17
	v_add_f32_e32 v64, v64, v98
	v_fmac_f32_e32 v68, v98, v33
	v_add_f32_e32 v65, v65, v100
	v_fmac_f32_e32 v69, v100, v36
	v_add_f32_e32 v82, v82, v100
	v_fmac_f32_e32 v86, v100, v19
	v_add_f32_e32 v66, v66, v102
	v_fmac_f32_e32 v70, v102, v35
	v_add_f32_e32 v81, v81, v102
	v_fmac_f32_e32 v85, v102, v20
	v_add_f32_e32 v67, v67, v97
	v_fmac_f32_e32 v71, v97, v38
	v_add_f32_e32 v83, v83, v99
	v_fmac_f32_e32 v87, v99, v22
	v_add_f32_e32 v80, v80, v101
	v_fmac_f32_e32 v84, v101, v25
	v_add_f32_e32 v72, v72, v103
	v_fmac_f32_e32 v76, v103, v33
	v_sub_f32_e64 v96, v38, v37
	v_fma_f32 v96, -v96, v96, s20
	s_nop 0
	v_exp_f32_e32 v96, v96
	v_add_f32_e32 v73, v73, v108
	v_fmac_f32_e32 v77, v108, v36
	v_add_f32_e32 v82, v82, v108
	v_fmac_f32_e32 v86, v108, v27
	v_add_f32_e32 v74, v74, v110
	v_fmac_f32_e32 v78, v110, v35
	v_add_f32_e32 v81, v81, v110
	v_fmac_f32_e32 v85, v110, v28
	v_add_f32_e32 v75, v75, v105
	v_fmac_f32_e32 v79, v105, v38
	v_add_f32_e32 v83, v83, v107
	v_fmac_f32_e32 v87, v107, v30
	v_add_f32_e32 v80, v80, v109
	v_fmac_f32_e32 v84, v109, v33
	v_add_f32_e32 v81, v81, v111
	v_fmac_f32_e32 v85, v111, v36
	v_add_f32_e32 v82, v82, v111
	v_fmac_f32_e32 v86, v111, v35
	v_pk_add_f32 v[80:81], v[80:81], v[104:105] op_sel_hi:[1,0]
	v_pk_fma_f32 v[84:85], v[104:105], v[34:35], v[84:85] op_sel:[0,1,0] op_sel_hi:[0,0,1]
	v_pk_add_f32 v[82:83], v[82:83], v[106:107] op_sel_hi:[1,0]
	v_pk_fma_f32 v[86:87], v[106:107], v[36:37], v[86:87] op_sel:[0,1,0] op_sel_hi:[0,0,1]
	s_nop 0
	v_add_f32_e32 v83, v83, v96
	v_fmac_f32_e32 v87, v96, v38
	s_waitcnt vmcnt(9)
	v_mov_b32_dpp v0, v4 row_shr:1 row_mask:0xf bank_mask:0xf
	v_mov_b32_dpp v1, v5 row_shr:1 row_mask:0xf bank_mask:0xf
	v_mov_b32_dpp v6, v2 row_shl:1 row_mask:0xf bank_mask:0xf
	v_mov_b32_dpp v7, v3 row_shl:1 row_mask:0xf bank_mask:0xf
	v_pk_mul_f32 v[2:3], v[2:3], s[32:33]
	v_pk_mul_f32 v[4:5], v[4:5], s[32:33]
	v_cndmask_b32_e64 v1, v1, v0, vcc
	v_cndmask_b32_e64 v6, v6, v7, s[16:17]
	v_pk_mul_f32 v[0:1], v[0:1], s[32:33]
	v_pk_mul_f32 v[6:7], v[6:7], s[32:33]
	s_setprio 2
	s_nop 0
	v_pk_add_f32 v[96:97], v[18:19], v[0:1] neg_lo:[0,1] neg_hi:[0,1]
	v_pk_add_f32 v[98:99], v[18:19], v[2:3] neg_lo:[0,1] neg_hi:[0,1]
	v_pk_add_f32 v[100:101], v[20:21], v[2:3] neg_lo:[0,1] neg_hi:[0,1]
	v_pk_add_f32 v[102:103], v[18:19], v[4:5] neg_lo:[0,1] neg_hi:[0,1]
	v_pk_fma_f32 v[96:97], v[96:97], v[96:97], s[28:29] neg_lo:[1,0,0] neg_hi:[1,0,0]
	v_pk_fma_f32 v[98:99], v[98:99], v[98:99], s[22:23] neg_lo:[1,0,0] neg_hi:[1,0,0]
	v_pk_fma_f32 v[100:101], v[100:101], v[100:101], s[28:29] neg_lo:[1,0,0] neg_hi:[1,0,0]
	v_pk_fma_f32 v[102:103], v[102:103], v[102:103], s[28:29] neg_lo:[1,0,0] neg_hi:[1,0,0]
	v_exp_f32_e32 v96, v96
	v_exp_f32_e32 v97, v97
	v_exp_f32_e32 v98, v98
	v_exp_f32_e32 v99, v99
	v_exp_f32_e32 v100, v100
	v_exp_f32_e32 v101, v101
	v_exp_f32_e32 v102, v102
	v_exp_f32_e32 v103, v103
	v_pk_add_f32 v[104:105], v[20:21], v[4:5] neg_lo:[0,1] neg_hi:[0,1]
	v_pk_add_f32 v[106:107], v[20:21], v[6:7] neg_lo:[0,1] neg_hi:[0,1]
	v_pk_add_f32 v[108:109], v[18:19], v[2:3] op_sel:[1,0] op_sel_hi:[0,1] neg_lo:[0,1] neg_hi:[0,1]
	v_pk_add_f32 v[110:111], v[20:21], v[4:5] op_sel:[1,0] op_sel_hi:[0,1] neg_lo:[0,1] neg_hi:[0,1]
	v_pk_fma_f32 v[104:105], v[104:105], v[104:105], s[22:23] neg_lo:[1,0,0] neg_hi:[1,0,0]
	v_pk_fma_f32 v[106:107], v[106:107], v[106:107], s[28:29] neg_lo:[1,0,0] neg_hi:[1,0,0]
	v_pk_fma_f32 v[108:109], v[108:109], v[108:109], s[26:27] neg_lo:[1,0,0] neg_hi:[1,0,0]
	v_pk_fma_f32 v[110:111], v[110:111], v[110:111], s[26:27] neg_lo:[1,0,0] neg_hi:[1,0,0]
	v_exp_f32_e32 v104, v104
	v_exp_f32_e32 v105, v105
	v_exp_f32_e32 v106, v106
	v_exp_f32_e32 v107, v107
	v_exp_f32_e32 v108, v108
	v_exp_f32_e32 v109, v109
	v_exp_f32_e32 v110, v110
	v_exp_f32_e32 v111, v111
	v_pk_add_f32 v[64:65], v[64:65], v[96:97]
	v_pk_fma_f32 v[68:69], v[96:97], v[0:1], v[68:69]
	v_pk_add_f32 v[66:67], v[66:67], v[100:101]
	v_pk_add_f32 v[64:65], v[64:65], v[98:99]
	v_pk_fma_f32 v[68:69], v[98:99], v[2:3], v[68:69]
	v_pk_fma_f32 v[70:71], v[100:101], v[2:3], v[70:71]
	v_pk_add_f32 v[64:65], v[64:65], v[102:103]
	v_pk_fma_f32 v[68:69], v[102:103], v[4:5], v[68:69]
	v_sub_f32_e32 v96, v18, v1
	v_sub_f32_e32 v98, v20, v3
	v_sub_f32_e32 v100, v19, v4
	v_sub_f32_e32 v102, v21, v6
	v_fma_f32 v96, -v96, v96, s26
	v_fma_f32 v98, -v98, v98, s26
	v_fma_f32 v100, -v100, v100, s26
	v_fma_f32 v102, -v102, v102, s26
	v_exp_f32_e32 v96, v96
	v_exp_f32_e32 v98, v98
	v_exp_f32_e32 v100, v100
	v_exp_f32_e32 v102, v102
	v_pk_add_f32 v[66:67], v[66:67], v[104:105]
	v_pk_fma_f32 v[70:71], v[104:105], v[4:5], v[70:71]
	v_pk_add_f32 v[64:65], v[64:65], v[108:109] op_sel:[0,1] op_sel_hi:[1,0]
	v_pk_add_f32 v[66:67], v[66:67], v[106:107]
	v_pk_fma_f32 v[70:71], v[106:107], v[6:7], v[70:71]
	v_pk_fma_f32 v[68:69], v[108:109], v[2:3], v[68:69] op_sel:[1,1,0] op_sel_hi:[0,0,1]
	v_pk_add_f32 v[66:67], v[66:67], v[110:111] op_sel:[0,1] op_sel_hi:[1,0]
	v_pk_fma_f32 v[70:71], v[110:111], v[4:5], v[70:71] op_sel:[1,1,0] op_sel_hi:[0,0,1]
	v_add_f32_e32 v64, v64, v96
	v_fmac_f32_e32 v68, v96, v1
	v_add_f32_e32 v66, v66, v98
	v_fmac_f32_e32 v70, v98, v3
	v_add_f32_e32 v65, v65, v100
	v_fmac_f32_e32 v69, v100, v4
	v_add_f32_e32 v67, v67, v102
	v_fmac_f32_e32 v71, v102, v6
	v_rcp_f32_e32 v96, v64
	v_rcp_f32_e32 v97, v65
	v_rcp_f32_e32 v98, v66
	v_rcp_f32_e32 v99, v67
	v_pk_mul_f32 v[68:69], v[68:69], s[34:35]
	v_pk_mul_f32 v[70:71], v[70:71], s[34:35]
	v_pk_mul_f32 v[68:69], v[68:69], v[96:97]
	v_pk_mul_f32 v[70:71], v[70:71], v[98:99]
	s_nop 0
	s_nop 0
	buffer_store_dwordx4 v[68:71], v114, s[12:15], 0 offen sc1
	s_waitcnt vmcnt(7)
	s_nop 0
	v_mov_b32_dpp v40, v44 row_shr:1 row_mask:0xf bank_mask:0xf
	v_mov_b32_dpp v41, v45 row_shr:1 row_mask:0xf bank_mask:0xf
	v_mov_b32_dpp v46, v42 row_shl:1 row_mask:0xf bank_mask:0xf
	v_mov_b32_dpp v47, v43 row_shl:1 row_mask:0xf bank_mask:0xf
	v_pk_mul_f32 v[42:43], v[42:43], s[32:33]
	v_pk_mul_f32 v[44:45], v[44:45], s[32:33]
	v_cndmask_b32_e64 v41, v41, v40, vcc
	v_cndmask_b32_e64 v46, v46, v47, s[16:17]
	v_pk_mul_f32 v[92:93], v[42:43], s[30:31]
	v_pk_mul_f32 v[94:95], v[44:45], s[30:31]
	v_pk_mul_f32 v[40:41], v[40:41], s[32:33]
	v_pk_mul_f32 v[46:47], v[46:47], s[32:33]
	v_mov_b32_e32 v88, s30
	v_mov_b32_e32 v89, s30
	v_mov_b32_e64 v90, s30
	v_mov_b32_e32 v91, s30
	s_setprio 1
	v_pk_add_f32 v[96:97], v[42:43], v[24:25] neg_lo:[0,1] neg_hi:[0,1]
	v_pk_add_f32 v[98:99], v[40:41], v[26:27] neg_lo:[0,1] neg_hi:[0,1]
	v_pk_add_f32 v[100:101], v[42:43], v[26:27] neg_lo:[0,1] neg_hi:[0,1]
	v_pk_add_f32 v[102:103], v[44:45], v[26:27] neg_lo:[0,1] neg_hi:[0,1]
	v_pk_fma_f32 v[96:97], v[96:97], v[96:97], s[28:29] neg_lo:[1,0,0] neg_hi:[1,0,0]
	v_pk_fma_f32 v[98:99], v[98:99], v[98:99], s[28:29] neg_lo:[1,0,0] neg_hi:[1,0,0]
	v_pk_fma_f32 v[100:101], v[100:101], v[100:101], s[22:23] neg_lo:[1,0,0] neg_hi:[1,0,0]
	v_pk_fma_f32 v[102:103], v[102:103], v[102:103], s[28:29] neg_lo:[1,0,0] neg_hi:[1,0,0]
	v_exp_f32_e32 v96, v96
	v_exp_f32_e32 v97, v97
	v_exp_f32_e32 v98, v98
	v_exp_f32_e32 v99, v99
	v_exp_f32_e32 v100, v100
	v_exp_f32_e32 v101, v101
	v_exp_f32_e32 v102, v102
	v_exp_f32_e32 v103, v103
	v_pk_add_f32 v[104:105], v[42:43], v[28:29] neg_lo:[0,1] neg_hi:[0,1]
	v_pk_add_f32 v[106:107], v[44:45], v[28:29] neg_lo:[0,1] neg_hi:[0,1]
	v_pk_add_f32 v[108:109], v[46:47], v[28:29] neg_lo:[0,1] neg_hi:[0,1]
	v_pk_add_f32 v[110:111], v[44:45], v[30:31] neg_lo:[0,1] neg_hi:[0,1]
	v_pk_fma_f32 v[104:105], v[104:105], v[104:105], s[28:29] neg_lo:[1,0,0] neg_hi:[1,0,0]
	v_pk_fma_f32 v[106:107], v[106:107], v[106:107], s[22:23] neg_lo:[1,0,0] neg_hi:[1,0,0]
	v_pk_fma_f32 v[108:109], v[108:109], v[108:109], s[28:29] neg_lo:[1,0,0] neg_hi:[1,0,0]
	v_pk_fma_f32 v[110:111], v[110:111], v[110:111], s[28:29] neg_lo:[1,0,0] neg_hi:[1,0,0]
	v_exp_f32_e32 v104, v104
	v_exp_f32_e32 v105, v105
	v_exp_f32_e32 v106, v106
	v_exp_f32_e32 v107, v107
	v_exp_f32_e32 v108, v108
	v_exp_f32_e32 v109, v109
	v_exp_f32_e32 v110, v110
	v_exp_f32_e32 v111, v111
	v_pk_add_f32 v[88:89], v[88:89], v[96:97]
	v_pk_fma_f32 v[92:93], v[96:97], v[24:25], v[92:93]
	v_pk_add_f32 v[72:73], v[72:73], v[98:99]
	v_pk_fma_f32 v[76:77], v[98:99], v[40:41], v[76:77]
	v_pk_add_f32 v[88:89], v[88:89], v[100:101]
	v_pk_add_f32 v[72:73], v[72:73], v[100:101]
	v_pk_fma_f32 v[76:77], v[100:101], v[42:43], v[76:77]
	v_pk_fma_f32 v[92:93], v[100:101], v[26:27], v[92:93]
	v_pk_add_f32 v[72:73], v[72:73], v[102:103]
	v_pk_fma_f32 v[76:77], v[102:103], v[44:45], v[76:77]
	v_pk_add_f32 v[90:91], v[90:91], v[102:103]
	v_pk_fma_f32 v[94:95], v[102:103], v[26:27], v[94:95]
	v_pk_add_f32 v[96:97], v[42:43], v[26:27] op_sel:[1,0] op_sel_hi:[0,1] neg_lo:[0,1] neg_hi:[0,1]
	v_pk_add_f32 v[98:99], v[44:45], v[28:29] op_sel:[1,0] op_sel_hi:[0,1] neg_lo:[0,1] neg_hi:[0,1]
	v_pk_add_f32 v[100:101], v[42:43], v[32:33] neg_lo:[0,1] neg_hi:[0,1]
	v_pk_add_f32 v[102:103], v[40:41], v[34:35] neg_lo:[0,1] neg_hi:[0,1]
	v_pk_fma_f32 v[96:97], v[96:97], v[96:97], s[26:27] neg_lo:[1,0,0] neg_hi:[1,0,0]
	v_pk_fma_f32 v[98:99], v[98:99], v[98:99], s[26:27] neg_lo:[1,0,0] neg_hi:[1,0,0]
	v_pk_fma_f32 v[100:101], v[100:101], v[100:101], s[26:27] neg_lo:[1,0,0] neg_hi:[1,0,0]
	v_pk_fma_f32 v[102:103], v[102:103], v[102:103], s[26:27] neg_lo:[1,0,0] neg_hi:[1,0,0]
	v_exp_f32_e32 v96, v96
	v_exp_f32_e32 v97, v97
	v_exp_f32_e32 v98, v98
	v_exp_f32_e32 v99, v99
	v_exp_f32_e32 v100, v100
	v_exp_f32_e32 v101, v101
	v_exp_f32_e32 v102, v102
	v_exp_f32_e32 v103, v103
	v_pk_add_f32 v[74:75], v[74:75], v[104:105]
	v_pk_fma_f32 v[78:79], v[104:105], v[42:43], v[78:79]
	v_pk_add_f32 v[88:89], v[88:89], v[104:105]
	v_pk_fma_f32 v[92:93], v[104:105], v[28:29], v[92:93]
	v_pk_add_f32 v[74:75], v[74:75], v[106:107]
	v_pk_fma_f32 v[78:79], v[106:107], v[44:45], v[78:79]
	v_pk_add_f32 v[90:91], v[90:91], v[106:107]
	v_pk_fma_f32 v[94:95], v[106:107], v[28:29], v[94:95]
	v_pk_add_f32 v[74:75], v[74:75], v[108:109]
	v_pk_fma_f32 v[78:79], v[108:109], v[46:47], v[78:79]
	v_pk_add_f32 v[90:91], v[90:91], v[110:111]
	v_pk_fma_f32 v[94:95], v[110:111], v[30:31], v[94:95]
	v_pk_add_f32 v[104:105], v[42:43], v[34:35] neg_lo:[0,1] neg_hi:[0,1]
	v_pk_add_f32 v[106:107], v[44:45], v[34:35] neg_lo:[0,1] neg_hi:[0,1]
	v_pk_add_f32 v[108:109], v[42:43], v[36:37] neg_lo:[0,1] neg_hi:[0,1]
	v_pk_add_f32 v[110:111], v[44:45], v[36:37] neg_lo:[0,1] neg_hi:[0,1]
	v_pk_fma_f32 v[104:105], v[104:105], v[104:105], s[20:21] neg_lo:[1,0,0] neg_hi:[1,0,0]
	v_pk_fma_f32 v[106:107], v[106:107], v[106:107], s[26:27] neg_lo:[1,0,0] neg_hi:[1,0,0]
	v_pk_fma_f32 v[108:109], v[108:109], v[108:109], s[26:27] neg_lo:[1,0,0] neg_hi:[1,0,0]
	v_pk_fma_f32 v[110:111], v[110:111], v[110:111], s[20:21] neg_lo:[1,0,0] neg_hi:[1,0,0]
	v_exp_f32_e32 v104, v104
	v_exp_f32_e32 v105, v105
	v_exp_f32_e32 v106, v106
	v_exp_f32_e32 v107, v107
	v_exp_f32_e32 v108, v108
	v_exp_f32_e32 v109, v109
	v_exp_f32_e32 v110, v110
	v_exp_f32_e32 v111, v111
	v_pk_add_f32 v[72:73], v[72:73], v[96:97]
	v_pk_fma_f32 v[76:77], v[96:97], v[42:43], v[76:77] op_sel:[0,1,0] op_sel_hi:[1,0,1]
	v_pk_add_f32 v[88:89], v[88:89], v[96:97] op_sel:[0,1] op_sel_hi:[1,0]
	v_pk_fma_f32 v[92:93], v[96:97], v[26:27], v[92:93] op_sel:[1,1,0] op_sel_hi:[0,0,1]
	v_pk_add_f32 v[74:75], v[74:75], v[98:99]
	v_pk_fma_f32 v[78:79], v[98:99], v[44:45], v[78:79] op_sel:[0,1,0] op_sel_hi:[1,0,1]
	v_pk_add_f32 v[90:91], v[90:91], v[98:99] op_sel:[0,1] op_sel_hi:[1,0]
	v_pk_fma_f32 v[94:95], v[98:99], v[28:29], v[94:95] op_sel:[1,1,0] op_sel_hi:[0,0,1]
	v_pk_add_f32 v[88:89], v[88:89], v[100:101]
	v_pk_fma_f32 v[92:93], v[100:101], v[32:33], v[92:93]
	v_pk_add_f32 v[80:81], v[80:81], v[102:103]
	v_pk_fma_f32 v[84:85], v[102:103], v[40:41], v[84:85]
	v_pk_add_f32 v[96:97], v[46:47], v[36:37] neg_lo:[0,1] neg_hi:[0,1]
	v_pk_add_f32 v[98:99], v[44:45], v[38:39] neg_lo:[0,1] neg_hi:[0,1]
	v_pk_add_f32 v[100:101], v[42:43], v[34:35] op_sel:[1,0] op_sel_hi:[0,1] neg_lo:[0,1] neg_hi:[0,1]
	v_pk_add_f32 v[102:103], v[44:45], v[36:37] op_sel:[1,0] op_sel_hi:[0,1] neg_lo:[0,1] neg_hi:[0,1]
	v_pk_fma_f32 v[96:97], v[96:97], v[96:97], s[26:27] neg_lo:[1,0,0] neg_hi:[1,0,0]
	v_pk_fma_f32 v[98:99], v[98:99], v[98:99], s[26:27] neg_lo:[1,0,0] neg_hi:[1,0,0]
	v_pk_fma_f32 v[100:101], v[100:101], v[100:101], s[24:25] neg_lo:[1,0,0] neg_hi:[1,0,0]
	v_pk_fma_f32 v[102:103], v[102:103], v[102:103], s[24:25] neg_lo:[1,0,0] neg_hi:[1,0,0]
	v_exp_f32_e32 v96, v96
	v_exp_f32_e32 v97, v97
	v_exp_f32_e32 v98, v98
	v_exp_f32_e32 v99, v99
	v_exp_f32_e32 v100, v100
	v_exp_f32_e32 v101, v101
	v_exp_f32_e32 v102, v102
	v_exp_f32_e32 v103, v103
	v_pk_add_f32 v[80:81], v[80:81], v[104:105]
	v_pk_fma_f32 v[84:85], v[104:105], v[42:43], v[84:85]
	v_pk_add_f32 v[88:89], v[88:89], v[104:105]
	v_pk_fma_f32 v[92:93], v[104:105], v[34:35], v[92:93]
	v_pk_add_f32 v[80:81], v[80:81], v[106:107]
	v_pk_fma_f32 v[84:85], v[106:107], v[44:45], v[84:85]
	v_pk_add_f32 v[90:91], v[90:91], v[106:107]
	v_pk_fma_f32 v[94:95], v[106:107], v[34:35], v[94:95]
	v_pk_add_f32 v[82:83], v[82:83], v[108:109]
	v_pk_fma_f32 v[86:87], v[108:109], v[42:43], v[86:87]
	v_pk_add_f32 v[88:89], v[88:89], v[108:109]
	v_pk_fma_f32 v[92:93], v[108:109], v[36:37], v[92:93]
	v_pk_add_f32 v[82:83], v[82:83], v[110:111]
	v_pk_fma_f32 v[86:87], v[110:111], v[44:45], v[86:87]
	v_pk_add_f32 v[90:91], v[90:91], v[110:111]
	v_pk_fma_f32 v[94:95], v[110:111], v[36:37], v[94:95]
	v_pk_add_f32 v[104:105], v[42:43], v[40:41] neg_lo:[0,1] neg_hi:[0,1]
	v_pk_add_f32 v[106:107], v[44:45], v[42:43] neg_lo:[0,1] neg_hi:[0,1]
	v_pk_add_f32 v[108:109], v[46:47], v[44:45] neg_lo:[0,1] neg_hi:[0,1]
	v_pk_fma_f32 v[104:105], v[104:105], v[104:105], s[22:23] neg_lo:[1,0,0] neg_hi:[1,0,0]
	v_pk_fma_f32 v[106:107], v[106:107], v[106:107], s[22:23] neg_lo:[1,0,0] neg_hi:[1,0,0]
	v_pk_fma_f32 v[108:109], v[108:109], v[108:109], s[22:23] neg_lo:[1,0,0] neg_hi:[1,0,0]
	v_exp_f32_e32 v104, v104
	v_exp_f32_e32 v105, v105
	v_exp_f32_e32 v106, v106
	v_exp_f32_e32 v107, v107
	v_exp_f32_e32 v108, v108
	v_exp_f32_e32 v109, v109
	v_pk_add_f32 v[82:83], v[82:83], v[96:97]
	v_pk_fma_f32 v[86:87], v[96:97], v[46:47], v[86:87]
	v_pk_add_f32 v[90:91], v[90:91], v[98:99]
	v_pk_fma_f32 v[94:95], v[98:99], v[38:39], v[94:95]
	v_pk_add_f32 v[80:81], v[80:81], v[100:101]
	v_pk_fma_f32 v[84:85], v[100:101], v[42:43], v[84:85] op_sel:[0,1,0] op_sel_hi:[1,0,1]
	v_pk_add_f32 v[88:89], v[88:89], v[100:101] op_sel:[0,1] op_sel_hi:[1,0]
	v_pk_fma_f32 v[92:93], v[100:101], v[34:35], v[92:93] op_sel:[1,1,0] op_sel_hi:[0,0,1]
	v_pk_add_f32 v[82:83], v[82:83], v[102:103]
	v_pk_fma_f32 v[86:87], v[102:103], v[44:45], v[86:87] op_sel:[0,1,0] op_sel_hi:[1,0,1]
	v_pk_add_f32 v[90:91], v[90:91], v[102:103] op_sel:[0,1] op_sel_hi:[1,0]
	v_pk_fma_f32 v[94:95], v[102:103], v[36:37], v[94:95] op_sel:[1,1,0] op_sel_hi:[0,0,1]
	v_sub_f32_e32 v96, v42, v25
	v_sub_f32_e32 v98, v41, v26
	v_sub_f32_e32 v100, v44, v27
	v_sub_f32_e32 v102, v43, v28
	v_sub_f32_e32 v97, v46, v29
	v_sub_f32_e32 v99, v45, v30
	v_sub_f32_e32 v101, v42, v33
	v_sub_f32_e32 v103, v41, v34
	v_fma_f32 v96, -v96, v96, s26
	v_fma_f32 v98, -v98, v98, s26
	v_fma_f32 v100, -v100, v100, s26
	v_fma_f32 v102, -v102, v102, s26
	v_fma_f32 v97, -v97, v97, s26
	v_fma_f32 v99, -v99, v99, s26
	v_fma_f32 v101, -v101, v101, s24
	v_fma_f32 v103, -v103, v103, s24
	v_exp_f32_e32 v96, v96
	v_exp_f32_e32 v98, v98
	v_exp_f32_e32 v100, v100
	v_exp_f32_e32 v102, v102
	v_exp_f32_e32 v97, v97
	v_exp_f32_e32 v99, v99
	v_exp_f32_e32 v101, v101
	v_exp_f32_e32 v103, v103
	v_pk_add_f32 v[88:89], v[88:89], v[104:105]
	v_pk_fma_f32 v[92:93], v[104:105], v[40:41], v[92:93]
	v_pk_add_f32 v[90:91], v[90:91], v[106:107]
	v_pk_add_f32 v[88:89], v[88:89], v[106:107]
	v_pk_fma_f32 v[92:93], v[106:107], v[44:45], v[92:93]
	v_pk_fma_f32 v[94:95], v[106:107], v[42:43], v[94:95]
	v_pk_add_f32 v[90:91], v[90:91], v[108:109]
	v_pk_fma_f32 v[94:95], v[108:109], v[46:47], v[94:95]
	v_sub_f32_e32 v108, v44, v35
	v_sub_f32_e32 v110, v43, v36
	v_sub_f32_e32 v105, v46, v37
	v_sub_f32_e32 v107, v45, v38
	v_sub_f32_e32 v109, v42, v41
	v_sub_f32_e32 v104, v43, v42
	v_sub_f32_e32 v111, v44, v43
	v_sub_f32_e32 v106, v45, v44
	v_fma_f32 v108, -v108, v108, s24
	v_fma_f32 v110, -v110, v110, s24
	v_fma_f32 v105, -v105, v105, s24
	v_fma_f32 v107, -v107, v107, s24
	v_fma_f32 v109, -v109, v109, s20
	v_fma_f32 v104, -v104, v104, s20
	v_fma_f32 v111, -v111, v111, s20
	v_fma_f32 v106, -v106, v106, s20
	v_exp_f32_e32 v108, v108
	v_exp_f32_e32 v110, v110
	v_exp_f32_e32 v105, v105
	v_exp_f32_e32 v107, v107
	v_exp_f32_e32 v109, v109
	v_exp_f32_e32 v104, v104
	v_exp_f32_e32 v111, v111
	v_exp_f32_e32 v106, v106
	v_add_f32_e32 v88, v88, v96
	v_fmac_f32_e32 v92, v96, v25
	v_add_f32_e32 v72, v72, v98
	v_fmac_f32_e32 v76, v98, v41
	v_add_f32_e32 v73, v73, v100
	v_fmac_f32_e32 v77, v100, v44
	v_add_f32_e32 v90, v90, v100
	v_fmac_f32_e32 v94, v100, v27
	v_add_f32_e32 v74, v74, v102
	v_fmac_f32_e32 v78, v102, v43
	v_add_f32_e32 v89, v89, v102
	v_fmac_f32_e32 v93, v102, v28
	v_add_f32_e32 v75, v75, v97
	v_fmac_f32_e32 v79, v97, v46
	v_add_f32_e32 v91, v91, v99
	v_fmac_f32_e32 v95, v99, v30
	v_add_f32_e32 v88, v88, v101
	v_fmac_f32_e32 v92, v101, v33
	v_add_f32_e32 v80, v80, v103
	v_fmac_f32_e32 v84, v103, v41
	v_sub_f32_e64 v96, v46, v45
	v_fma_f32 v96, -v96, v96, s20
	s_nop 0
	v_exp_f32_e32 v96, v96
	v_add_f32_e32 v81, v81, v108
	v_fmac_f32_e32 v85, v108, v44
	v_add_f32_e32 v90, v90, v108
	v_fmac_f32_e32 v94, v108, v35
	v_add_f32_e32 v82, v82, v110
	v_fmac_f32_e32 v86, v110, v43
	v_add_f32_e32 v89, v89, v110
	v_fmac_f32_e32 v93, v110, v36
	v_add_f32_e32 v83, v83, v105
	v_fmac_f32_e32 v87, v105, v46
	v_add_f32_e32 v91, v91, v107
	v_fmac_f32_e32 v95, v107, v38
	v_add_f32_e32 v88, v88, v109
	v_fmac_f32_e32 v92, v109, v41
	v_add_f32_e32 v89, v89, v111
	v_fmac_f32_e32 v93, v111, v44
	v_add_f32_e32 v90, v90, v111
	v_fmac_f32_e32 v94, v111, v43
	v_pk_add_f32 v[88:89], v[88:89], v[104:105] op_sel_hi:[1,0]
	v_pk_fma_f32 v[92:93], v[104:105], v[42:43], v[92:93] op_sel:[0,1,0] op_sel_hi:[0,0,1]
	v_pk_add_f32 v[90:91], v[90:91], v[106:107] op_sel_hi:[1,0]
	v_pk_fma_f32 v[94:95], v[106:107], v[44:45], v[94:95] op_sel:[0,1,0] op_sel_hi:[0,0,1]
	s_nop 0
	v_add_f32_e32 v91, v91, v96
	v_fmac_f32_e32 v95, v96, v46
	v_rcp_f32_e32 v96, v72
	v_rcp_f32_e32 v97, v73
	v_rcp_f32_e32 v98, v74
	v_rcp_f32_e64 v99, v75
	v_pk_mul_f32 v[76:77], v[76:77], s[34:35]
	v_pk_mul_f32 v[78:79], v[78:79], s[34:35]
	v_pk_mul_f32 v[76:77], v[76:77], v[96:97]
	v_pk_mul_f32 v[78:79], v[78:79], v[98:99]
	s_nop 0
	s_nop 0
	buffer_store_dwordx4 v[76:79], v114, s[12:15], 0 offen offset:2048 sc1
	s_waitcnt vmcnt(5)
	s_nop 0
	v_mov_b32_dpp v48, v52 row_shr:1 row_mask:0xf bank_mask:0xf
	v_mov_b32_dpp v49, v53 row_shr:1 row_mask:0xf bank_mask:0xf
	v_mov_b32_dpp v54, v50 row_shl:1 row_mask:0xf bank_mask:0xf
	v_mov_b32_dpp v55, v51 row_shl:1 row_mask:0xf bank_mask:0xf
	v_pk_mul_f32 v[50:51], v[50:51], s[32:33]
	v_pk_mul_f32 v[52:53], v[52:53], s[32:33]
	v_cndmask_b32_e64 v49, v49, v48, vcc
	v_cndmask_b32_e64 v54, v54, v55, s[16:17]
	v_pk_mul_f32 v[48:49], v[48:49], s[32:33]
	v_pk_mul_f32 v[54:55], v[54:55], s[32:33]
	s_setprio 0
	s_nop 0
	v_pk_add_f32 v[96:97], v[48:49], v[34:35] neg_lo:[0,1] neg_hi:[0,1]
	v_pk_add_f32 v[98:99], v[50:51], v[34:35] neg_lo:[0,1] neg_hi:[0,1]
	v_pk_add_f32 v[100:101], v[52:53], v[34:35] neg_lo:[0,1] neg_hi:[0,1]
	v_pk_add_f32 v[102:103], v[50:51], v[36:37] neg_lo:[0,1] neg_hi:[0,1]
	v_pk_fma_f32 v[96:97], v[96:97], v[96:97], s[28:29] neg_lo:[1,0,0] neg_hi:[1,0,0]
	v_pk_fma_f32 v[98:99], v[98:99], v[98:99], s[22:23] neg_lo:[1,0,0] neg_hi:[1,0,0]
	v_pk_fma_f32 v[100:101], v[100:101], v[100:101], s[28:29] neg_lo:[1,0,0] neg_hi:[1,0,0]
	v_pk_fma_f32 v[102:103], v[102:103], v[102:103], s[28:29] neg_lo:[1,0,0] neg_hi:[1,0,0]
	v_exp_f32_e32 v96, v96
	v_exp_f32_e32 v97, v97
	v_exp_f32_e32 v98, v98
	v_exp_f32_e32 v99, v99
	v_exp_f32_e32 v100, v100
	v_exp_f32_e32 v101, v101
	v_exp_f32_e32 v102, v102
	v_exp_f32_e32 v103, v103
	v_pk_add_f32 v[104:105], v[52:53], v[36:37] neg_lo:[0,1] neg_hi:[0,1]
	v_pk_add_f32 v[106:107], v[54:55], v[36:37] neg_lo:[0,1] neg_hi:[0,1]
	v_pk_add_f32 v[108:109], v[50:51], v[34:35] op_sel:[1,0] op_sel_hi:[0,1] neg_lo:[0,1] neg_hi:[0,1]
	v_pk_add_f32 v[110:111], v[52:53], v[36:37] op_sel:[1,0] op_sel_hi:[0,1] neg_lo:[0,1] neg_hi:[0,1]
	v_pk_fma_f32 v[104:105], v[104:105], v[104:105], s[22:23] neg_lo:[1,0,0] neg_hi:[1,0,0]
	v_pk_fma_f32 v[106:107], v[106:107], v[106:107], s[28:29] neg_lo:[1,0,0] neg_hi:[1,0,0]
	v_pk_fma_f32 v[108:109], v[108:109], v[108:109], s[26:27] neg_lo:[1,0,0] neg_hi:[1,0,0]
	v_pk_fma_f32 v[110:111], v[110:111], v[110:111], s[26:27] neg_lo:[1,0,0] neg_hi:[1,0,0]
	v_exp_f32_e32 v104, v104
	v_exp_f32_e32 v105, v105
	v_exp_f32_e32 v106, v106
	v_exp_f32_e32 v107, v107
	v_exp_f32_e32 v108, v108
	v_exp_f32_e32 v109, v109
	v_exp_f32_e32 v110, v110
	v_exp_f32_e32 v111, v111
	v_pk_add_f32 v[80:81], v[80:81], v[96:97]
	v_pk_fma_f32 v[84:85], v[96:97], v[48:49], v[84:85]
	v_pk_add_f32 v[82:83], v[82:83], v[102:103]
	v_pk_add_f32 v[80:81], v[80:81], v[98:99]
	v_pk_fma_f32 v[84:85], v[98:99], v[50:51], v[84:85]
	v_pk_fma_f32 v[86:87], v[102:103], v[50:51], v[86:87]
	v_pk_add_f32 v[80:81], v[80:81], v[100:101]
	v_pk_fma_f32 v[84:85], v[100:101], v[52:53], v[84:85]
	v_pk_add_f32 v[96:97], v[48:49], v[42:43] neg_lo:[0,1] neg_hi:[0,1]
	v_pk_add_f32 v[98:99], v[50:51], v[42:43] neg_lo:[0,1] neg_hi:[0,1]
	v_pk_add_f32 v[100:101], v[52:53], v[42:43] neg_lo:[0,1] neg_hi:[0,1]
	v_pk_add_f32 v[102:103], v[50:51], v[44:45] neg_lo:[0,1] neg_hi:[0,1]
	v_pk_fma_f32 v[96:97], v[96:97], v[96:97], s[26:27] neg_lo:[1,0,0] neg_hi:[1,0,0]
	v_pk_fma_f32 v[98:99], v[98:99], v[98:99], s[20:21] neg_lo:[1,0,0] neg_hi:[1,0,0]
	v_pk_fma_f32 v[100:101], v[100:101], v[100:101], s[26:27] neg_lo:[1,0,0] neg_hi:[1,0,0]
	v_pk_fma_f32 v[102:103], v[102:103], v[102:103], s[26:27] neg_lo:[1,0,0] neg_hi:[1,0,0]
	v_exp_f32_e32 v96, v96
	v_exp_f32_e32 v97, v97
	v_exp_f32_e32 v98, v98
	v_exp_f32_e32 v99, v99
	v_exp_f32_e32 v100, v100
	v_exp_f32_e32 v101, v101
	v_exp_f32_e32 v102, v102
	v_exp_f32_e32 v103, v103
	v_pk_add_f32 v[82:83], v[82:83], v[104:105]
	v_pk_fma_f32 v[86:87], v[104:105], v[52:53], v[86:87]
	v_pk_add_f32 v[80:81], v[80:81], v[108:109]
	v_pk_add_f32 v[82:83], v[82:83], v[106:107]
	v_pk_fma_f32 v[86:87], v[106:107], v[54:55], v[86:87]
	v_pk_fma_f32 v[84:85], v[108:109], v[50:51], v[84:85] op_sel:[0,1,0] op_sel_hi:[1,0,1]
	v_pk_add_f32 v[82:83], v[82:83], v[110:111]
	v_pk_fma_f32 v[86:87], v[110:111], v[52:53], v[86:87] op_sel:[0,1,0] op_sel_hi:[1,0,1]
	v_pk_add_f32 v[104:105], v[52:53], v[44:45] neg_lo:[0,1] neg_hi:[0,1]
	v_pk_add_f32 v[106:107], v[54:55], v[44:45] neg_lo:[0,1] neg_hi:[0,1]
	v_pk_add_f32 v[108:109], v[50:51], v[42:43] op_sel:[1,0] op_sel_hi:[0,1] neg_lo:[0,1] neg_hi:[0,1]
	v_pk_add_f32 v[110:111], v[52:53], v[44:45] op_sel:[1,0] op_sel_hi:[0,1] neg_lo:[0,1] neg_hi:[0,1]
	v_pk_fma_f32 v[104:105], v[104:105], v[104:105], s[20:21] neg_lo:[1,0,0] neg_hi:[1,0,0]
	v_pk_fma_f32 v[106:107], v[106:107], v[106:107], s[26:27] neg_lo:[1,0,0] neg_hi:[1,0,0]
	v_pk_fma_f32 v[108:109], v[108:109], v[108:109], s[24:25] neg_lo:[1,0,0] neg_hi:[1,0,0]
	v_pk_fma_f32 v[110:111], v[110:111], v[110:111], s[24:25] neg_lo:[1,0,0] neg_hi:[1,0,0]
	v_exp_f32_e32 v104, v104
	v_exp_f32_e32 v105, v105
	v_exp_f32_e32 v106, v106
	v_exp_f32_e32 v107, v107
	v_exp_f32_e32 v108, v108
	v_exp_f32_e32 v109, v109
	v_exp_f32_e32 v110, v110
	v_exp_f32_e32 v111, v111
	v_pk_add_f32 v[88:89], v[88:89], v[96:97]
	v_pk_fma_f32 v[92:93], v[96:97], v[48:49], v[92:93]
	v_pk_add_f32 v[90:91], v[90:91], v[102:103]
	v_pk_add_f32 v[88:89], v[88:89], v[98:99]
	v_pk_fma_f32 v[92:93], v[98:99], v[50:51], v[92:93]
	v_pk_fma_f32 v[94:95], v[102:103], v[50:51], v[94:95]
	v_pk_add_f32 v[88:89], v[88:89], v[100:101]
	v_pk_fma_f32 v[92:93], v[100:101], v[52:53], v[92:93]
	v_sub_f32_e32 v96, v49, v34
	v_sub_f32_e32 v98, v52, v35
	v_sub_f32_e32 v100, v51, v36
	v_sub_f32_e32 v102, v54, v37
	v_sub_f32_e32 v97, v49, v42
	v_sub_f32_e32 v99, v52, v43
	v_sub_f32_e32 v101, v51, v44
	v_sub_f32_e32 v103, v54, v45
	v_fma_f32 v96, -v96, v96, s26
	v_fma_f32 v98, -v98, v98, s26
	v_fma_f32 v100, -v100, v100, s26
	v_fma_f32 v102, -v102, v102, s26
	v_fma_f32 v97, -v97, v97, s24
	v_fma_f32 v99, -v99, v99, s24
	v_fma_f32 v101, -v101, v101, s24
	v_fma_f32 v103, -v103, v103, s24
	v_exp_f32_e32 v96, v96
	v_exp_f32_e32 v98, v98
	v_exp_f32_e32 v100, v100
	v_exp_f32_e32 v102, v102
	v_exp_f32_e32 v97, v97
	v_exp_f32_e32 v99, v99
	v_exp_f32_e32 v101, v101
	v_exp_f32_e32 v103, v103
	v_pk_add_f32 v[90:91], v[90:91], v[104:105]
	v_pk_fma_f32 v[94:95], v[104:105], v[52:53], v[94:95]
	v_pk_add_f32 v[88:89], v[88:89], v[108:109]
	v_pk_add_f32 v[90:91], v[90:91], v[106:107]
	v_pk_fma_f32 v[94:95], v[106:107], v[54:55], v[94:95]
	v_pk_fma_f32 v[92:93], v[108:109], v[50:51], v[92:93] op_sel:[0,1,0] op_sel_hi:[1,0,1]
	v_pk_add_f32 v[90:91], v[90:91], v[110:111]
	v_pk_fma_f32 v[94:95], v[110:111], v[52:53], v[94:95] op_sel:[0,1,0] op_sel_hi:[1,0,1]
	v_add_f32_e32 v80, v80, v96
	v_fmac_f32_e32 v84, v96, v49
	v_add_f32_e32 v81, v81, v98
	v_fmac_f32_e32 v85, v98, v52
	v_add_f32_e32 v82, v82, v100
	v_fmac_f32_e32 v86, v100, v51
	v_add_f32_e32 v83, v83, v102
	v_fmac_f32_e32 v87, v102, v54
	v_add_f32_e32 v88, v88, v97
	v_fmac_f32_e32 v92, v97, v49
	v_add_f32_e32 v89, v89, v99
	v_fmac_f32_e32 v93, v99, v52
	v_add_f32_e32 v90, v90, v101
	v_fmac_f32_e32 v94, v101, v51
	v_add_f32_e32 v91, v91, v103
	v_fmac_f32_e32 v95, v103, v54
	v_rcp_f32_e32 v96, v80
	v_rcp_f32_e32 v97, v81
	v_rcp_f32_e32 v98, v82
	v_rcp_f32_e32 v99, v83
	v_pk_mul_f32 v[84:85], v[84:85], s[34:35]
	v_pk_mul_f32 v[86:87], v[86:87], s[34:35]
	v_pk_mul_f32 v[84:85], v[84:85], v[96:97]
	v_pk_mul_f32 v[86:87], v[86:87], v[98:99]
	s_nop 0
	s_nop 0
	buffer_store_dwordx4 v[84:87], v119, s[12:15], 0 offen sc1
	s_waitcnt vmcnt(3)
	s_nop 0
	v_mov_b32_dpp v56, v60 row_shr:1 row_mask:0xf bank_mask:0xf
	v_mov_b32_dpp v57, v61 row_shr:1 row_mask:0xf bank_mask:0xf
	v_mov_b32_dpp v62, v58 row_shl:1 row_mask:0xf bank_mask:0xf
	v_mov_b32_dpp v63, v59 row_shl:1 row_mask:0xf bank_mask:0xf
	v_pk_mul_f32 v[58:59], v[58:59], s[32:33]
	v_pk_mul_f32 v[60:61], v[60:61], s[32:33]
	v_cndmask_b32_e64 v57, v57, v56, vcc
	v_cndmask_b32_e64 v62, v62, v63, s[16:17]
	v_pk_mul_f32 v[56:57], v[56:57], s[32:33]
	v_pk_mul_f32 v[62:63], v[62:63], s[32:33]
	s_setprio 0
	s_nop 0
	v_pk_add_f32 v[96:97], v[56:57], v[42:43] neg_lo:[0,1] neg_hi:[0,1]
	v_pk_add_f32 v[98:99], v[58:59], v[42:43] neg_lo:[0,1] neg_hi:[0,1]
	v_pk_add_f32 v[100:101], v[60:61], v[42:43] neg_lo:[0,1] neg_hi:[0,1]
	v_pk_add_f32 v[102:103], v[58:59], v[44:45] neg_lo:[0,1] neg_hi:[0,1]
	v_pk_fma_f32 v[96:97], v[96:97], v[96:97], s[28:29] neg_lo:[1,0,0] neg_hi:[1,0,0]
	v_pk_fma_f32 v[98:99], v[98:99], v[98:99], s[22:23] neg_lo:[1,0,0] neg_hi:[1,0,0]
	v_pk_fma_f32 v[100:101], v[100:101], v[100:101], s[28:29] neg_lo:[1,0,0] neg_hi:[1,0,0]
	v_pk_fma_f32 v[102:103], v[102:103], v[102:103], s[28:29] neg_lo:[1,0,0] neg_hi:[1,0,0]
	v_exp_f32_e32 v96, v96
	v_exp_f32_e32 v97, v97
	v_exp_f32_e32 v98, v98
	v_exp_f32_e32 v99, v99
	v_exp_f32_e32 v100, v100
	v_exp_f32_e32 v101, v101
	v_exp_f32_e32 v102, v102
	v_exp_f32_e32 v103, v103
	v_pk_add_f32 v[104:105], v[60:61], v[44:45] neg_lo:[0,1] neg_hi:[0,1]
	v_pk_add_f32 v[106:107], v[62:63], v[44:45] neg_lo:[0,1] neg_hi:[0,1]
	v_pk_add_f32 v[108:109], v[58:59], v[42:43] op_sel:[1,0] op_sel_hi:[0,1] neg_lo:[0,1] neg_hi:[0,1]
	v_pk_add_f32 v[110:111], v[60:61], v[44:45] op_sel:[1,0] op_sel_hi:[0,1] neg_lo:[0,1] neg_hi:[0,1]
	v_pk_fma_f32 v[104:105], v[104:105], v[104:105], s[22:23] neg_lo:[1,0,0] neg_hi:[1,0,0]
	v_pk_fma_f32 v[106:107], v[106:107], v[106:107], s[28:29] neg_lo:[1,0,0] neg_hi:[1,0,0]
	v_pk_fma_f32 v[108:109], v[108:109], v[108:109], s[26:27] neg_lo:[1,0,0] neg_hi:[1,0,0]
	v_pk_fma_f32 v[110:111], v[110:111], v[110:111], s[26:27] neg_lo:[1,0,0] neg_hi:[1,0,0]
	v_exp_f32_e32 v104, v104
	v_exp_f32_e32 v105, v105
	v_exp_f32_e32 v106, v106
	v_exp_f32_e32 v107, v107
	v_exp_f32_e32 v108, v108
	v_exp_f32_e32 v109, v109
	v_exp_f32_e32 v110, v110
	v_exp_f32_e32 v111, v111
	v_pk_add_f32 v[88:89], v[88:89], v[96:97]
	v_pk_fma_f32 v[92:93], v[96:97], v[56:57], v[92:93]
	v_pk_add_f32 v[90:91], v[90:91], v[102:103]
	v_pk_add_f32 v[88:89], v[88:89], v[98:99]
	v_pk_fma_f32 v[92:93], v[98:99], v[58:59], v[92:93]
	v_pk_fma_f32 v[94:95], v[102:103], v[58:59], v[94:95]
	v_pk_add_f32 v[88:89], v[88:89], v[100:101]
	v_pk_fma_f32 v[92:93], v[100:101], v[60:61], v[92:93]
	v_sub_f32_e32 v96, v57, v42
	v_sub_f32_e32 v98, v60, v43
	v_sub_f32_e32 v100, v59, v44
	v_sub_f32_e32 v102, v62, v45
	v_fma_f32 v96, -v96, v96, s26
	v_fma_f32 v98, -v98, v98, s26
	v_fma_f32 v100, -v100, v100, s26
	v_fma_f32 v102, -v102, v102, s26
	v_exp_f32_e32 v96, v96
	v_exp_f32_e32 v98, v98
	v_exp_f32_e32 v100, v100
	v_exp_f32_e32 v102, v102
	v_pk_add_f32 v[90:91], v[90:91], v[104:105]
	v_pk_fma_f32 v[94:95], v[104:105], v[60:61], v[94:95]
	v_pk_add_f32 v[88:89], v[88:89], v[108:109]
	v_pk_add_f32 v[90:91], v[90:91], v[106:107]
	v_pk_fma_f32 v[94:95], v[106:107], v[62:63], v[94:95]
	v_pk_fma_f32 v[92:93], v[108:109], v[58:59], v[92:93] op_sel:[0,1,0] op_sel_hi:[1,0,1]
	v_pk_add_f32 v[90:91], v[90:91], v[110:111]
	v_pk_fma_f32 v[94:95], v[110:111], v[60:61], v[94:95] op_sel:[0,1,0] op_sel_hi:[1,0,1]
	v_add_f32_e32 v88, v88, v96
	v_fmac_f32_e32 v92, v96, v57
	v_add_f32_e32 v89, v89, v98
	v_fmac_f32_e32 v93, v98, v60
	v_add_f32_e32 v90, v90, v100
	v_fmac_f32_e32 v94, v100, v59
	v_add_f32_e32 v91, v91, v102
	v_fmac_f32_e32 v95, v102, v62
	v_rcp_f32_e32 v96, v88
	v_rcp_f32_e32 v97, v89
	v_rcp_f32_e32 v98, v90
	v_rcp_f32_e32 v99, v91
	v_pk_mul_f32 v[92:93], v[92:93], s[34:35]
	v_pk_mul_f32 v[94:95], v[94:95], s[34:35]
	v_pk_mul_f32 v[92:93], v[92:93], v[96:97]
	v_pk_mul_f32 v[94:95], v[94:95], v[98:99]
	s_nop 0
	s_nop 0
	buffer_store_dwordx4 v[92:95], v119, s[12:15], 0 offen offset:2048 sc1
	s_endpgm
